# best + K-loop edge edits + duplicate post-barrier lgkmcnt(0) waits removed (placement of loop headers and downstream code preserved by pads)
# speedup vs baseline: 1.0102x; 1.0026x over previous
; #define G8_STAGE(bufoff, gbase, voff) do { _Pragma("unroll") for (int _i = 0; _i < 2; ++_i) \
;         __builtin_amdgcn_global_load_lds((const unsigned*)((const char*)(gbase) + (voff)[_i]), (LAS unsigned*)(lds + (bufoff) + ldsw + _i * 8192), 16, 0, 0); } while (0)
; #define G8_LDA(dst, b, h) do { _Pragma("unroll") for (int m = 0; m < 4; ++m) _Pragma("unroll") for (int k = 0; k < 2; ++k) dst[m][k] = *(const LAS bf16x8*)(lds + G8_SA(b, h) + aoff + m * 2048 + k * 1024); } while (0)
; #define G8_LDB(dst, b, h) do { _Pragma("unroll") for (int n = 0; n < 2; ++n) _Pragma("unroll") for (int k = 0; k < 2; ++k) dst[n][k] = *(const LAS bf16x8*)(lds + G8_SB(b, h) + boff + n * 2048 + k * 1024); } while (0)
; #define G8_MMA(ai, bj, At, Bt) do { __builtin_amdgcn_s_setprio(1); _Pragma("unroll") for (int m = 0; m < 4; ++m) _Pragma("unroll") for (int n = 0; n < 2; ++n) _Pragma("unroll") for (int k = 0; k < 2; ++k) \
;         acc[ai][bj][m][n] = __builtin_amdgcn_mfma_f32_16x16x32_bf16(Bt[n][k], At[m][k], acc[ai][bj][m][n], 0, 0, 0); __builtin_amdgcn_s_setprio(0); } while (0)
; #define G8_WAIT_L(n) asm volatile("s_waitcnt lgkmcnt(" #n ")" ::: "memory")
; #define G8_BAR __builtin_amdgcn_s_barrier()
; #define G8_SCHED __builtin_amdgcn_sched_barrier(0)
; template <class Epi, class Sched>
; __device__ __forceinline__ void gemm_phase(LAS unsigned char* lds, const int K, const Sched& S, const Epi& E) {
;     ...
;             const bool last = (t == nt - 2);
;             const char* a1 = cA + (size_t)(t + 1) * kstep;
;             const char* a2 = last ? nA : cA + (size_t)(t + 2) * kstep; const char* b2 = last ? nB : cB + (size_t)(t + 2) * kstep;
;             const char* a3 = a2 + kstep; const char* b3 = b2 + kstep;
;             G8_LDB(B0, 0, 0); G8_SCHED; G8_LDA(At, 0, 0); G8_STAGE(G8_SA(1, 1), a1, oc[1]);
;             if (last && has_next) S.aoff(nxt, tid, oc);
;             G8_WAIT_L(8); G8_BAR; G8_WAIT_L(0); G8_MMA(0, 0, At, B0); G8_BAR; G8_SCHED;
;             G8_LDB(B1, 0, 1); G8_STAGE(G8_SB(0, 0), b2, voffB);
;             G8_BAR; G8_WAIT_L(0); G8_MMA(0, 1, At, B1); G8_BAR;
;             G8_LDA(At, 0, 1); G8_STAGE(G8_SA(0, 0), a2, oc[0]);
;             G8_BAR; G8_WAIT_L(0); G8_MMA(1, 0, At, B0); G8_BAR; G8_SCHED;
.LBB0_320:
	s_add_u32 s36, s2, 0x100
	s_addc_u32 s37, s3, 0
	s_add_i32 s82, 0, 0x10000
	v_add_u32_e32 v0, s82, v145
	ds_read_b128 v[154:157], v0
	ds_read_b128 v[158:161], v0 offset:1024
	ds_read_b128 v[162:165], v0 offset:2048
	ds_read_b128 v[166:169], v0 offset:3072
	s_cmp_eq_u32 s11, 12
	s_cselect_b32 s49, s43, s37
	s_cselect_b32 s48, s42, s36
	s_cselect_b32 s47, s45, s9
	s_cselect_b32 s46, s44, s5
	v_lshl_add_u64 v[150:151], s[2:3], 0, v[148:149]
	s_add_i32 m0, s58, 0xc000
	ds_read_b128 v[170:173], v153
	ds_read_b128 v[174:177], v153 offset:1024
	ds_read_b128 v[178:181], v153 offset:2048
	ds_read_b128 v[182:185], v153 offset:3072
	ds_read_b128 v[186:189], v153 offset:4096
	ds_read_b128 v[190:193], v153 offset:5120
	ds_read_b128 v[194:197], v153 offset:6144
	ds_read_b128 v[198:201], v153 offset:7168
	global_load_lds_dwordx4 v[150:151], off
	v_lshl_add_u64 v[150:151], s[2:3], 0, v[146:147]
	s_add_i32 m0, s58, 0xe000
	s_nop 0
	global_load_lds_dwordx4 v[150:151], off
	s_waitcnt lgkmcnt(8)
	s_setprio 1
	s_barrier
	s_waitcnt lgkmcnt(0)
	v_mfma_f32_16x16x32_bf16 v[126:129], v[154:157], v[170:173], v[126:129]
	v_mfma_f32_16x16x32_bf16 v[122:125], v[162:165], v[170:173], v[122:125]
	v_mfma_f32_16x16x32_bf16 v[110:113], v[154:157], v[178:181], v[110:113]
	v_mfma_f32_16x16x32_bf16 v[106:109], v[162:165], v[178:181], v[106:109]
	v_mfma_f32_16x16x32_bf16 v[94:97], v[154:157], v[186:189], v[94:97]
	v_mfma_f32_16x16x32_bf16 v[90:93], v[162:165], v[186:189], v[90:93]
	v_mfma_f32_16x16x32_bf16 v[78:81], v[154:157], v[194:197], v[78:81]
	v_mfma_f32_16x16x32_bf16 v[74:77], v[162:165], v[194:197], v[74:77]
	v_mfma_f32_16x16x32_bf16 v[126:129], v[158:161], v[174:177], v[126:129]
	v_mfma_f32_16x16x32_bf16 v[122:125], v[166:169], v[174:177], v[122:125]
	v_mfma_f32_16x16x32_bf16 v[110:113], v[158:161], v[182:185], v[110:113]
	v_mfma_f32_16x16x32_bf16 v[106:109], v[166:169], v[182:185], v[106:109]
	v_mfma_f32_16x16x32_bf16 v[94:97], v[158:161], v[190:193], v[94:97]
	v_mfma_f32_16x16x32_bf16 v[90:93], v[166:169], v[190:193], v[90:93]
	v_mfma_f32_16x16x32_bf16 v[78:81], v[158:161], v[198:201], v[78:81]
	v_mfma_f32_16x16x32_bf16 v[74:77], v[166:169], v[198:201], v[74:77]
	s_setprio 0
	s_barrier
	s_add_i32 s83, 0, 0x14000
	s_add_i32 s2, s82, s57
	v_add_u32_e32 v0, s83, v145
	v_lshl_add_u64 v[150:151], s[46:47], 0, v[132:133]
	s_mov_b32 m0, s2
	ds_read_b128 v[216:219], v0
	ds_read_b128 v[220:223], v0 offset:1024
	ds_read_b128 v[224:227], v0 offset:2048
	ds_read_b128 v[228:231], v0 offset:3072
	global_load_lds_dwordx4 v[150:151], off
	v_lshl_add_u64 v[232:233], s[46:47], 0, v[134:135]
	s_add_i32 m0, s2, 0x2000
	s_nop 0
	global_load_lds_dwordx4 v[232:233], off
	s_setprio 1
	s_barrier
	s_waitcnt lgkmcnt(0)
	v_mfma_f32_16x16x32_bf16 v[118:121], v[216:219], v[170:173], v[118:121]
	v_mfma_f32_16x16x32_bf16 v[114:117], v[224:227], v[170:173], v[114:117]
	v_mfma_f32_16x16x32_bf16 v[102:105], v[216:219], v[178:181], v[102:105]
	v_mfma_f32_16x16x32_bf16 v[98:101], v[224:227], v[178:181], v[98:101]
	v_mfma_f32_16x16x32_bf16 v[86:89], v[216:219], v[186:189], v[86:89]
	v_mfma_f32_16x16x32_bf16 v[82:85], v[224:227], v[186:189], v[82:85]
	v_mfma_f32_16x16x32_bf16 v[70:73], v[216:219], v[194:197], v[70:73]
	v_mfma_f32_16x16x32_bf16 v[66:69], v[224:227], v[194:197], v[66:69]
	v_mfma_f32_16x16x32_bf16 v[118:121], v[220:223], v[174:177], v[118:121]
	s_mov_b32 m0, s58
	v_mfma_f32_16x16x32_bf16 v[114:117], v[228:231], v[174:177], v[114:117]
	v_lshl_add_u64 v[234:235], s[48:49], 0, v[136:137]
	v_mfma_f32_16x16x32_bf16 v[102:105], v[220:223], v[182:185], v[102:105]
	v_mfma_f32_16x16x32_bf16 v[98:101], v[228:231], v[182:185], v[98:101]
	v_mfma_f32_16x16x32_bf16 v[86:89], v[220:223], v[190:193], v[86:89]
	v_mfma_f32_16x16x32_bf16 v[82:85], v[228:231], v[190:193], v[82:85]
	v_mfma_f32_16x16x32_bf16 v[70:73], v[220:223], v[198:201], v[70:73]
	v_mfma_f32_16x16x32_bf16 v[66:69], v[228:231], v[198:201], v[66:69]
	s_setprio 0
	s_barrier
	ds_read_b128 v[170:173], v153 offset:16384
	ds_read_b128 v[174:177], v153 offset:17408
	ds_read_b128 v[178:181], v153 offset:18432
	ds_read_b128 v[182:185], v153 offset:19456
	ds_read_b128 v[186:189], v153 offset:20480
	ds_read_b128 v[190:193], v153 offset:21504
	ds_read_b128 v[194:197], v153 offset:22528
	ds_read_b128 v[198:201], v153 offset:23552
	global_load_lds_dwordx4 v[234:235], off
	v_lshl_add_u64 v[236:237], s[48:49], 0, v[140:141]
	s_mov_b32 m0, s59
	s_nop 0
	global_load_lds_dwordx4 v[236:237], off
	s_setprio 1
	s_barrier
	s_waitcnt lgkmcnt(0)
	v_mfma_f32_16x16x32_bf16 v[62:65], v[154:157], v[170:173], v[62:65]
	v_mfma_f32_16x16x32_bf16 v[58:61], v[162:165], v[170:173], v[58:61]
	v_mfma_f32_16x16x32_bf16 v[46:49], v[154:157], v[178:181], v[46:49]
	v_mfma_f32_16x16x32_bf16 v[42:45], v[162:165], v[178:181], v[42:45]
	v_mfma_f32_16x16x32_bf16 v[30:33], v[154:157], v[186:189], v[30:33]
	v_mfma_f32_16x16x32_bf16 v[26:29], v[162:165], v[186:189], v[26:29]
	v_mfma_f32_16x16x32_bf16 v[14:17], v[154:157], v[194:197], v[14:17]
	v_mfma_f32_16x16x32_bf16 v[10:13], v[162:165], v[194:197], v[10:13]
	v_mfma_f32_16x16x32_bf16 v[62:65], v[158:161], v[174:177], v[62:65]
	v_mfma_f32_16x16x32_bf16 v[58:61], v[166:169], v[174:177], v[58:61]
	v_mfma_f32_16x16x32_bf16 v[46:49], v[158:161], v[182:185], v[46:49]
	v_mfma_f32_16x16x32_bf16 v[42:45], v[166:169], v[182:185], v[42:45]
	v_mfma_f32_16x16x32_bf16 v[30:33], v[158:161], v[190:193], v[30:33]
	v_mfma_f32_16x16x32_bf16 v[26:29], v[166:169], v[190:193], v[26:29]
	v_mfma_f32_16x16x32_bf16 v[14:17], v[158:161], v[198:201], v[14:17]
	v_mfma_f32_16x16x32_bf16 v[10:13], v[166:169], v[198:201], v[10:13]
	s_setprio 0
	s_barrier
; #define G8_STAGE(bufoff, gbase, voff) do { _Pragma("unroll") for (int _i = 0; _i < 2; ++_i) \
;         __builtin_amdgcn_global_load_lds((const unsigned*)((const char*)(gbase) + (voff)[_i]), (LAS unsigned*)(lds + (bufoff) + ldsw + _i * 8192), 16, 0, 0); } while (0)
; #define G8_LDA(dst, b, h) do { _Pragma("unroll") for (int m = 0; m < 4; ++m) _Pragma("unroll") for (int k = 0; k < 2; ++k) dst[m][k] = *(const LAS bf16x8*)(lds + G8_SA(b, h) + aoff + m * 2048 + k * 1024); } while (0)
; #define G8_LDB(dst, b, h) do { _Pragma("unroll") for (int n = 0; n < 2; ++n) _Pragma("unroll") for (int k = 0; k < 2; ++k) dst[n][k] = *(const LAS bf16x8*)(lds + G8_SB(b, h) + boff + n * 2048 + k * 1024); } while (0)
; #define G8_MMA(ai, bj, At, Bt) do { __builtin_amdgcn_s_setprio(1); _Pragma("unroll") for (int m = 0; m < 4; ++m) _Pragma("unroll") for (int n = 0; n < 2; ++n) _Pragma("unroll") for (int k = 0; k < 2; ++k) \
;         acc[ai][bj][m][n] = __builtin_amdgcn_mfma_f32_16x16x32_bf16(Bt[n][k], At[m][k], acc[ai][bj][m][n], 0, 0, 0); __builtin_amdgcn_s_setprio(0); } while (0)
; #define G8_WAIT_V(n) asm volatile("s_waitcnt vmcnt(" #n ")" ::: "memory")
; #define G8_WAIT_L(n) asm volatile("s_waitcnt lgkmcnt(" #n ")" ::: "memory")
; #define G8_BAR __builtin_amdgcn_s_barrier()
; #define G8_SCHED __builtin_amdgcn_sched_barrier(0)
; template <class Epi, class Sched>
; __device__ __forceinline__ void gemm_phase(LAS unsigned char* lds, const int K, const Sched& S, const Epi& E) {
;     ...
;             G8_STAGE(G8_SB(0, 1), b2 + hstep, voffB);
;             G8_WAIT_V(6); G8_BAR; G8_MMA(1, 1, At, B1); G8_BAR;
;             G8_LDB(B0, 1, 0); G8_SCHED; G8_LDA(At, 1, 0); G8_STAGE(G8_SA(0, 1), a2, oc[1]);
;             G8_WAIT_L(8); G8_BAR; G8_WAIT_L(0); G8_MMA(0, 0, At, B0); G8_BAR; G8_SCHED;
;             G8_LDB(B1, 1, 1); G8_STAGE(G8_SB(1, 0), b3, voffB);
;             G8_BAR; G8_WAIT_L(0); G8_MMA(0, 1, At, B1); G8_BAR;
	s_add_u32 s2, s46, 0x40000
	s_addc_u32 s3, s47, 0
	s_add_i32 s82, s83, s57
	v_lshl_add_u64 v[154:155], s[2:3], 0, v[132:133]
	s_mov_b32 m0, s82
	s_nop 0
	global_load_lds_dwordx4 v[154:155], off
	v_lshl_add_u64 v[154:155], s[2:3], 0, v[134:135]
	s_add_i32 m0, s82, 0x2000
	s_nop 0
	global_load_lds_dwordx4 v[154:155], off
	s_waitcnt vmcnt(6)
	s_setprio 1
	s_barrier
	v_mfma_f32_16x16x32_bf16 v[54:57], v[216:219], v[170:173], v[54:57]
	v_mfma_f32_16x16x32_bf16 v[50:53], v[224:227], v[170:173], v[50:53]
	v_mfma_f32_16x16x32_bf16 v[38:41], v[216:219], v[178:181], v[38:41]
	v_mfma_f32_16x16x32_bf16 v[34:37], v[224:227], v[178:181], v[34:37]
	v_mfma_f32_16x16x32_bf16 v[22:25], v[216:219], v[186:189], v[22:25]
	v_mfma_f32_16x16x32_bf16 v[18:21], v[224:227], v[186:189], v[18:21]
	v_mfma_f32_16x16x32_bf16 v[6:9], v[216:219], v[194:197], v[6:9]
	v_mfma_f32_16x16x32_bf16 v[2:5], v[224:227], v[194:197], v[2:5]
	v_mfma_f32_16x16x32_bf16 v[54:57], v[220:223], v[174:177], v[54:57]
	s_add_i32 s2, 0, 0x18000
	v_mfma_f32_16x16x32_bf16 v[50:53], v[228:231], v[174:177], v[50:53]
	v_add_u32_e32 v0, s2, v145
	v_mfma_f32_16x16x32_bf16 v[38:41], v[220:223], v[182:185], v[38:41]
	v_mfma_f32_16x16x32_bf16 v[34:37], v[228:231], v[182:185], v[34:37]
	v_mfma_f32_16x16x32_bf16 v[22:25], v[220:223], v[190:193], v[22:25]
	v_mfma_f32_16x16x32_bf16 v[18:21], v[228:231], v[190:193], v[18:21]
	v_mfma_f32_16x16x32_bf16 v[6:9], v[220:223], v[198:201], v[6:9]
	v_mfma_f32_16x16x32_bf16 v[2:5], v[228:231], v[198:201], v[2:5]
	s_setprio 0
	s_barrier
	ds_read_b128 v[154:157], v0
	ds_read_b128 v[158:161], v0 offset:1024
	ds_read_b128 v[162:165], v0 offset:2048
	ds_read_b128 v[166:169], v0 offset:3072
	s_mov_b32 m0, s60
	v_lshl_add_u64 v[216:217], s[48:49], 0, v[138:139]
	ds_read_b128 v[170:173], v153 offset:32768
	ds_read_b128 v[174:177], v153 offset:33792
	ds_read_b128 v[178:181], v153 offset:34816
	ds_read_b128 v[182:185], v153 offset:35840
	ds_read_b128 v[186:189], v153 offset:36864
	ds_read_b128 v[190:193], v153 offset:37888
	ds_read_b128 v[194:197], v153 offset:38912
	ds_read_b128 v[198:201], v153 offset:39936
	global_load_lds_dwordx4 v[216:217], off
	v_lshl_add_u64 v[216:217], s[48:49], 0, v[142:143]
	s_mov_b32 m0, s61
	s_nop 0
	global_load_lds_dwordx4 v[216:217], off
	s_waitcnt lgkmcnt(8)
	s_setprio 1
	s_barrier
	s_waitcnt lgkmcnt(0)
	v_mfma_f32_16x16x32_bf16 v[126:129], v[154:157], v[170:173], v[126:129]
	v_mfma_f32_16x16x32_bf16 v[122:125], v[162:165], v[170:173], v[122:125]
	v_mfma_f32_16x16x32_bf16 v[110:113], v[154:157], v[178:181], v[110:113]
	v_mfma_f32_16x16x32_bf16 v[106:109], v[162:165], v[178:181], v[106:109]
	v_mfma_f32_16x16x32_bf16 v[94:97], v[154:157], v[186:189], v[94:97]
	v_mfma_f32_16x16x32_bf16 v[90:93], v[162:165], v[186:189], v[90:93]
	v_mfma_f32_16x16x32_bf16 v[78:81], v[154:157], v[194:197], v[78:81]
	v_mfma_f32_16x16x32_bf16 v[74:77], v[162:165], v[194:197], v[74:77]
	v_mfma_f32_16x16x32_bf16 v[126:129], v[158:161], v[174:177], v[126:129]
	v_mfma_f32_16x16x32_bf16 v[122:125], v[166:169], v[174:177], v[122:125]
	v_mfma_f32_16x16x32_bf16 v[110:113], v[158:161], v[182:185], v[110:113]
	v_mfma_f32_16x16x32_bf16 v[106:109], v[166:169], v[182:185], v[106:109]
	v_mfma_f32_16x16x32_bf16 v[94:97], v[158:161], v[190:193], v[94:97]
	v_mfma_f32_16x16x32_bf16 v[90:93], v[166:169], v[190:193], v[90:93]
	v_mfma_f32_16x16x32_bf16 v[78:81], v[158:161], v[198:201], v[78:81]
	v_mfma_f32_16x16x32_bf16 v[74:77], v[166:169], v[198:201], v[74:77]
	s_setprio 0
	s_barrier
	s_add_i32 s48, 0, 0x1c000
	s_add_i32 s2, s2, s57
	v_add_u32_e32 v0, s48, v145
	v_lshl_add_u64 v[150:151], v[150:151], 0, s[18:19]
	s_mov_b32 m0, s2
	ds_read_b128 v[216:219], v0
	ds_read_b128 v[220:223], v0 offset:1024
	ds_read_b128 v[224:227], v0 offset:2048
	ds_read_b128 v[228:231], v0 offset:3072
	global_load_lds_dwordx4 v[150:151], off
	v_lshl_add_u64 v[150:151], v[232:233], 0, s[18:19]
	s_add_i32 m0, s2, 0x2000
	s_nop 0
	global_load_lds_dwordx4 v[150:151], off
	s_setprio 1
	s_barrier
	s_waitcnt lgkmcnt(0)
	v_mfma_f32_16x16x32_bf16 v[118:121], v[216:219], v[170:173], v[118:121]
	v_mfma_f32_16x16x32_bf16 v[114:117], v[224:227], v[170:173], v[114:117]
	v_mfma_f32_16x16x32_bf16 v[102:105], v[216:219], v[178:181], v[102:105]
	v_mfma_f32_16x16x32_bf16 v[98:101], v[224:227], v[178:181], v[98:101]
	v_mfma_f32_16x16x32_bf16 v[86:89], v[216:219], v[186:189], v[86:89]
	v_mfma_f32_16x16x32_bf16 v[82:85], v[224:227], v[186:189], v[82:85]
	v_mfma_f32_16x16x32_bf16 v[70:73], v[216:219], v[194:197], v[70:73]
	v_mfma_f32_16x16x32_bf16 v[66:69], v[224:227], v[194:197], v[66:69]
	v_mfma_f32_16x16x32_bf16 v[118:121], v[220:223], v[174:177], v[118:121]
	s_mov_b32 m0, s64
	v_mfma_f32_16x16x32_bf16 v[114:117], v[228:231], v[174:177], v[114:117]
	v_lshl_add_u64 v[150:151], v[234:235], 0, s[18:19]
	v_mfma_f32_16x16x32_bf16 v[102:105], v[220:223], v[182:185], v[102:105]
	v_mfma_f32_16x16x32_bf16 v[98:101], v[228:231], v[182:185], v[98:101]
	v_mfma_f32_16x16x32_bf16 v[86:89], v[220:223], v[190:193], v[86:89]
	v_mfma_f32_16x16x32_bf16 v[82:85], v[228:231], v[190:193], v[82:85]
	v_mfma_f32_16x16x32_bf16 v[70:73], v[220:223], v[198:201], v[70:73]
	v_mfma_f32_16x16x32_bf16 v[66:69], v[228:231], v[198:201], v[66:69]
	s_setprio 0
	s_barrier
; #define G8_STAGE(bufoff, gbase, voff) do { _Pragma("unroll") for (int _i = 0; _i < 2; ++_i) \
;         __builtin_amdgcn_global_load_lds((const unsigned*)((const char*)(gbase) + (voff)[_i]), (LAS unsigned*)(lds + (bufoff) + ldsw + _i * 8192), 16, 0, 0); } while (0)
; #define G8_LDA(dst, b, h) do { _Pragma("unroll") for (int m = 0; m < 4; ++m) _Pragma("unroll") for (int k = 0; k < 2; ++k) dst[m][k] = *(const LAS bf16x8*)(lds + G8_SA(b, h) + aoff + m * 2048 + k * 1024); } while (0)
; #define G8_MMA(ai, bj, At, Bt) do { __builtin_amdgcn_s_setprio(1); _Pragma("unroll") for (int m = 0; m < 4; ++m) _Pragma("unroll") for (int n = 0; n < 2; ++n) _Pragma("unroll") for (int k = 0; k < 2; ++k) \
;         acc[ai][bj][m][n] = __builtin_amdgcn_mfma_f32_16x16x32_bf16(Bt[n][k], At[m][k], acc[ai][bj][m][n], 0, 0, 0); __builtin_amdgcn_s_setprio(0); } while (0)
; #define G8_WAIT_V(n) asm volatile("s_waitcnt vmcnt(" #n ")" ::: "memory")
; #define G8_WAIT_L(n) asm volatile("s_waitcnt lgkmcnt(" #n ")" ::: "memory")
; #define G8_BAR __builtin_amdgcn_s_barrier()
; #define G8_SCHED __builtin_amdgcn_sched_barrier(0)
; __device__ __forceinline__ f32x4 gelu4(const f32x4 x) {
;     const f32x4 t = x * ((x * x) * (-0.10294323886f) + (-2.30220819813f)); f32x4 d;
; #pragma unroll
;     for (int e = 0; e < 4; ++e) d[e] = __builtin_amdgcn_exp2f(t[e]);
;     d = d + 1.f;
; #pragma unroll
;     for (int e = 0; e < 4; ++e) d[e] = __builtin_amdgcn_rcpf(d[e]);
;     return x * d; }
; template <class Epi, class Sched>
; __device__ __forceinline__ void gemm_phase(LAS unsigned char* lds, const int K, const Sched& S, const Epi& E) {
;     ...
;             G8_LDA(At, 1, 1); G8_STAGE(G8_SA(1, 0), a3, oc[0]);
;             G8_BAR; G8_WAIT_L(0); G8_MMA(1, 0, At, B0); G8_BAR; G8_SCHED;
;             G8_STAGE(G8_SB(1, 1), b3 + hstep, voffB);
;             G8_WAIT_V(6); G8_BAR; G8_MMA(1, 1, At, B1); G8_BAR;
;         }
;         E(acc, cur, wr, wc, fr, fq);
	ds_read_b128 v[170:173], v153 offset:49152
	ds_read_b128 v[174:177], v153 offset:50176
	ds_read_b128 v[178:181], v153 offset:51200
	ds_read_b128 v[182:185], v153 offset:52224
	ds_read_b128 v[186:189], v153 offset:53248
	ds_read_b128 v[190:193], v153 offset:54272
	ds_read_b128 v[194:197], v153 offset:55296
	ds_read_b128 v[198:201], v153 offset:56320
	global_load_lds_dwordx4 v[150:151], off
	v_lshl_add_u64 v[150:151], v[236:237], 0, s[18:19]
	s_mov_b32 m0, s65
	s_nop 0
	global_load_lds_dwordx4 v[150:151], off
	s_setprio 1
	s_barrier
	s_waitcnt lgkmcnt(0)
	v_mfma_f32_16x16x32_bf16 v[62:65], v[154:157], v[170:173], v[62:65]
	v_mfma_f32_16x16x32_bf16 v[58:61], v[162:165], v[170:173], v[58:61]
	v_mfma_f32_16x16x32_bf16 v[46:49], v[154:157], v[178:181], v[46:49]
	v_mfma_f32_16x16x32_bf16 v[42:45], v[162:165], v[178:181], v[42:45]
	v_mfma_f32_16x16x32_bf16 v[30:33], v[154:157], v[186:189], v[30:33]
	v_mfma_f32_16x16x32_bf16 v[26:29], v[162:165], v[186:189], v[26:29]
	v_mfma_f32_16x16x32_bf16 v[14:17], v[154:157], v[194:197], v[14:17]
	v_mfma_f32_16x16x32_bf16 v[10:13], v[162:165], v[194:197], v[10:13]
	v_mfma_f32_16x16x32_bf16 v[62:65], v[158:161], v[174:177], v[62:65]
	v_mfma_f32_16x16x32_bf16 v[58:61], v[166:169], v[174:177], v[58:61]
	v_mfma_f32_16x16x32_bf16 v[46:49], v[158:161], v[182:185], v[46:49]
	v_mfma_f32_16x16x32_bf16 v[42:45], v[166:169], v[182:185], v[42:45]
	v_mfma_f32_16x16x32_bf16 v[30:33], v[158:161], v[190:193], v[30:33]
	v_mfma_f32_16x16x32_bf16 v[26:29], v[166:169], v[190:193], v[26:29]
	v_mfma_f32_16x16x32_bf16 v[14:17], v[158:161], v[198:201], v[14:17]
	v_mfma_f32_16x16x32_bf16 v[10:13], v[166:169], v[198:201], v[10:13]
	s_setprio 0
	s_barrier
	s_add_u32 s2, s46, 0x40080
	s_addc_u32 s3, s47, 0
	s_add_i32 s46, s48, s57
	v_lshl_add_u64 v[150:151], s[2:3], 0, v[132:133]
	s_mov_b32 m0, s46
	s_nop 0
	global_load_lds_dwordx4 v[150:151], off
	v_lshl_add_u64 v[150:151], s[2:3], 0, v[134:135]
	s_add_i32 m0, s46, 0x2000
	s_nop 0
	global_load_lds_dwordx4 v[150:151], off
	s_waitcnt vmcnt(6)
	s_setprio 1
	s_barrier
	v_mfma_f32_16x16x32_bf16 v[54:57], v[216:219], v[170:173], v[54:57]
	v_mfma_f32_16x16x32_bf16 v[50:53], v[224:227], v[170:173], v[50:53]
	v_mfma_f32_16x16x32_bf16 v[38:41], v[216:219], v[178:181], v[38:41]
	v_mfma_f32_16x16x32_bf16 v[34:37], v[224:227], v[178:181], v[34:37]
	v_mfma_f32_16x16x32_bf16 v[22:25], v[216:219], v[186:189], v[22:25]
	v_mfma_f32_16x16x32_bf16 v[18:21], v[224:227], v[186:189], v[18:21]
	v_mfma_f32_16x16x32_bf16 v[6:9], v[216:219], v[194:197], v[6:9]
	v_mfma_f32_16x16x32_bf16 v[2:5], v[224:227], v[194:197], v[2:5]
	v_mfma_f32_16x16x32_bf16 v[54:57], v[220:223], v[174:177], v[54:57]
	s_add_i32 s11, s11, 2
	v_mfma_f32_16x16x32_bf16 v[50:53], v[228:231], v[174:177], v[50:53]
	s_add_u32 s5, s5, 0x100
	v_mfma_f32_16x16x32_bf16 v[38:41], v[220:223], v[182:185], v[38:41]
	s_addc_u32 s9, s9, 0
	v_mfma_f32_16x16x32_bf16 v[34:37], v[228:231], v[182:185], v[34:37]
	s_cmp_gt_u32 s11, 13
	v_mfma_f32_16x16x32_bf16 v[22:25], v[220:223], v[190:193], v[22:25]
	s_mov_b64 s[2:3], s[36:37]
	v_mfma_f32_16x16x32_bf16 v[18:21], v[228:231], v[190:193], v[18:21]
	v_mfma_f32_16x16x32_bf16 v[6:9], v[220:223], v[198:201], v[6:9]
	v_mfma_f32_16x16x32_bf16 v[2:5], v[228:231], v[198:201], v[2:5]
	s_setprio 0
	s_barrier
	s_cbranch_scc0 .LBB0_320
	s_nop 0
	s_nop 0
	s_nop 0
	s_nop 0
	s_nop 0
	s_nop 0
	s_nop 0
	s_nop 0
	s_nop 0
	s_nop 0
	s_nop 0
	s_nop 0
	s_nop 0
	s_nop 0
	s_nop 0
	s_nop 0
	s_nop 0
	s_cmp_lt_i32 s14, 13
	s_cselect_b64 s[36:37], -1, 0
	s_and_b64 vcc, exec, s[36:37]
	s_cbranch_vccz .LBB0_325
	v_pk_mul_f32 v[154:155], v[126:127], v[126:127]
	v_pk_mul_f32 v[150:151], v[128:129], v[128:129]
	v_fmamk_f32 v0, v154, 0xbdd2d3e8, v202
	v_mul_f32_e32 v0, v126, v0
	v_exp_f32_e32 v154, v0
	v_fmamk_f32 v0, v155, 0xbdd2d3e8, v202
	v_mul_f32_e32 v0, v127, v0
	v_exp_f32_e32 v155, v0
	v_fmamk_f32 v0, v150, 0xbdd2d3e8, v202
	v_mul_f32_e32 v0, v128, v0
	v_exp_f32_e32 v150, v0
	v_fmamk_f32 v0, v151, 0xbdd2d3e8, v202
	v_mul_f32_e32 v0, v129, v0
	v_exp_f32_e32 v151, v0
	v_pk_add_f32 v[154:155], v[154:155], 1.0 op_sel_hi:[1,0]
	v_pk_add_f32 v[150:151], v[150:151], 1.0 op_sel_hi:[1,0]
	v_rcp_f32_e32 v154, v154
	v_rcp_f32_e32 v155, v155
	v_rcp_f32_e32 v150, v150
	v_rcp_f32_e32 v151, v151
	v_pk_mul_f32 v[126:127], v[126:127], v[154:155]
	v_pk_mul_f32 v[128:129], v[128:129], v[150:151]
	v_cndmask_b32_e64 v0, 0, 1, s[36:37]
	v_cmp_ne_u32_e64 s[2:3], 1, v0
	s_andn2_b64 vcc, exec, s[36:37]
	s_cbranch_vccz .LBB0_326

; #define G8_STAGE(bufoff, gbase, voff) do { _Pragma("unroll") for (int _i = 0; _i < 2; ++_i) \
;         __builtin_amdgcn_global_load_lds((const unsigned*)((const char*)(gbase) + (voff)[_i]), (LAS unsigned*)(lds + (bufoff) + ldsw + _i * 8192), 16, 0, 0); } while (0)
; #define G8_LDA(dst, b, h) do { _Pragma("unroll") for (int m = 0; m < 4; ++m) _Pragma("unroll") for (int k = 0; k < 2; ++k) dst[m][k] = *(const LAS bf16x8*)(lds + G8_SA(b, h) + aoff + m * 2048 + k * 1024); } while (0)
; #define G8_LDB(dst, b, h) do { _Pragma("unroll") for (int n = 0; n < 2; ++n) _Pragma("unroll") for (int k = 0; k < 2; ++k) dst[n][k] = *(const LAS bf16x8*)(lds + G8_SB(b, h) + boff + n * 2048 + k * 1024); } while (0)
; #define G8_MMA(ai, bj, At, Bt) do { __builtin_amdgcn_s_setprio(1); _Pragma("unroll") for (int m = 0; m < 4; ++m) _Pragma("unroll") for (int n = 0; n < 2; ++n) _Pragma("unroll") for (int k = 0; k < 2; ++k) \
;         acc[ai][bj][m][n] = __builtin_amdgcn_mfma_f32_16x16x32_bf16(Bt[n][k], At[m][k], acc[ai][bj][m][n], 0, 0, 0); __builtin_amdgcn_s_setprio(0); } while (0)
; #define G8_WAIT_L(n) asm volatile("s_waitcnt lgkmcnt(" #n ")" ::: "memory")
; #define G8_BAR __builtin_amdgcn_s_barrier()
; #define G8_SCHED __builtin_amdgcn_sched_barrier(0)
; template <class Epi, class Sched>
; __device__ __forceinline__ void gemm_phase(LAS unsigned char* lds, const int K, const Sched& S, const Epi& E) {
;     ...
;             const bool last = (t == nt - 2);
;             const char* a1 = cA + (size_t)(t + 1) * kstep;
;             const char* a2 = last ? nA : cA + (size_t)(t + 2) * kstep; const char* b2 = last ? nB : cB + (size_t)(t + 2) * kstep;
;             const char* a3 = a2 + kstep; const char* b3 = b2 + kstep;
;             G8_LDB(B0, 0, 0); G8_SCHED; G8_LDA(At, 0, 0); G8_STAGE(G8_SA(1, 1), a1, oc[1]);
;             if (last && has_next) S.aoff(nxt, tid, oc);
;             G8_WAIT_L(8); G8_BAR; G8_WAIT_L(0); G8_MMA(0, 0, At, B0); G8_BAR; G8_SCHED;
;             G8_LDB(B1, 0, 1); G8_STAGE(G8_SB(0, 0), b2, voffB);
;             G8_BAR; G8_WAIT_L(0); G8_MMA(0, 1, At, B1); G8_BAR;
;             G8_LDA(At, 0, 1); G8_STAGE(G8_SA(0, 0), a2, oc[0]);
;             G8_BAR; G8_WAIT_L(0); G8_MMA(1, 0, At, B0); G8_BAR; G8_SCHED;
.LBB0_487:
	s_add_u32 s12, s0, 0x100
	s_addc_u32 s13, s1, 0
	s_add_i32 s49, 0, 0x10000
	v_add_u32_e32 v158, s49, v165
	ds_read_b128 v[130:133], v158
	ds_read_b128 v[134:137], v158 offset:1024
	ds_read_b128 v[154:157], v158 offset:2048
	ds_read_b128 v[158:161], v158 offset:3072
	s_cmp_eq_u32 s47, 12
	s_cselect_b32 s43, s23, s13
	s_cselect_b32 s42, s22, s12
	s_cselect_b32 s39, s37, s14
	s_cselect_b32 s38, s36, s3
	v_lshl_add_u64 v[162:163], s[0:1], 0, v[152:153]
	s_add_i32 m0, s76, 0xc000
	ds_read_b128 v[168:171], v167
	ds_read_b128 v[172:175], v167 offset:1024
	ds_read_b128 v[176:179], v167 offset:2048
	ds_read_b128 v[180:183], v167 offset:3072
	ds_read_b128 v[184:187], v167 offset:4096
	ds_read_b128 v[188:191], v167 offset:5120
	ds_read_b128 v[192:195], v167 offset:6144
	ds_read_b128 v[196:199], v167 offset:7168
	global_load_lds_dwordx4 v[162:163], off
	v_lshl_add_u64 v[162:163], s[0:1], 0, v[150:151]
	s_add_i32 m0, s76, 0xe000
	s_nop 0
	global_load_lds_dwordx4 v[162:163], off
	s_waitcnt lgkmcnt(8)
	s_setprio 1
	s_barrier
	s_waitcnt lgkmcnt(0)
	v_mfma_f32_16x16x32_bf16 v[126:129], v[130:133], v[168:171], v[126:129]
	v_mfma_f32_16x16x32_bf16 v[118:121], v[154:157], v[168:171], v[118:121]
	v_mfma_f32_16x16x32_bf16 v[110:113], v[130:133], v[176:179], v[110:113]
	v_mfma_f32_16x16x32_bf16 v[102:105], v[154:157], v[176:179], v[102:105]
	v_mfma_f32_16x16x32_bf16 v[94:97], v[130:133], v[184:187], v[94:97]
	v_mfma_f32_16x16x32_bf16 v[86:89], v[154:157], v[184:187], v[86:89]
	v_mfma_f32_16x16x32_bf16 v[78:81], v[130:133], v[192:195], v[78:81]
	v_mfma_f32_16x16x32_bf16 v[70:73], v[154:157], v[192:195], v[70:73]
	v_mfma_f32_16x16x32_bf16 v[126:129], v[134:137], v[172:175], v[126:129]
	v_mfma_f32_16x16x32_bf16 v[118:121], v[158:161], v[172:175], v[118:121]
	v_mfma_f32_16x16x32_bf16 v[110:113], v[134:137], v[180:183], v[110:113]
	v_mfma_f32_16x16x32_bf16 v[102:105], v[158:161], v[180:183], v[102:105]
	v_mfma_f32_16x16x32_bf16 v[94:97], v[134:137], v[188:191], v[94:97]
	v_mfma_f32_16x16x32_bf16 v[86:89], v[158:161], v[188:191], v[86:89]
	v_mfma_f32_16x16x32_bf16 v[78:81], v[134:137], v[196:199], v[78:81]
	v_mfma_f32_16x16x32_bf16 v[70:73], v[158:161], v[196:199], v[70:73]
	s_setprio 0
	s_barrier
	s_add_i32 s54, 0, 0x14000
	v_add_u32_e32 v162, s54, v165
	s_add_i32 s0, s49, s65
	ds_read_b128 v[216:219], v162
	ds_read_b128 v[220:223], v162 offset:1024
	ds_read_b128 v[224:227], v162 offset:2048
	ds_read_b128 v[228:231], v162 offset:3072
	v_lshl_add_u64 v[162:163], s[38:39], 0, v[0:1]
	s_mov_b32 m0, s0
	v_lshl_add_u64 v[200:201], s[38:39], 0, v[140:141]
	global_load_lds_dwordx4 v[162:163], off
	s_add_i32 m0, s0, 0x2000
	s_nop 0
	global_load_lds_dwordx4 v[200:201], off
	s_setprio 1
	s_barrier
	s_waitcnt lgkmcnt(0)
	v_mfma_f32_16x16x32_bf16 v[122:125], v[216:219], v[168:171], v[122:125]
	v_mfma_f32_16x16x32_bf16 v[114:117], v[224:227], v[168:171], v[114:117]
	v_mfma_f32_16x16x32_bf16 v[106:109], v[216:219], v[176:179], v[106:109]
	v_mfma_f32_16x16x32_bf16 v[98:101], v[224:227], v[176:179], v[98:101]
	v_mfma_f32_16x16x32_bf16 v[90:93], v[216:219], v[184:187], v[90:93]
	v_mfma_f32_16x16x32_bf16 v[82:85], v[224:227], v[184:187], v[82:85]
	v_mfma_f32_16x16x32_bf16 v[74:77], v[216:219], v[192:195], v[74:77]
	v_mfma_f32_16x16x32_bf16 v[66:69], v[224:227], v[192:195], v[66:69]
	v_mfma_f32_16x16x32_bf16 v[122:125], v[220:223], v[172:175], v[122:125]
	s_mov_b32 m0, s76
	v_mfma_f32_16x16x32_bf16 v[114:117], v[228:231], v[172:175], v[114:117]
	v_lshl_add_u64 v[232:233], s[42:43], 0, v[142:143]
	v_mfma_f32_16x16x32_bf16 v[106:109], v[220:223], v[180:183], v[106:109]
	v_mfma_f32_16x16x32_bf16 v[98:101], v[228:231], v[180:183], v[98:101]
	v_mfma_f32_16x16x32_bf16 v[90:93], v[220:223], v[188:191], v[90:93]
	v_mfma_f32_16x16x32_bf16 v[82:85], v[228:231], v[188:191], v[82:85]
	v_mfma_f32_16x16x32_bf16 v[74:77], v[220:223], v[196:199], v[74:77]
	v_mfma_f32_16x16x32_bf16 v[66:69], v[228:231], v[196:199], v[66:69]
	s_setprio 0
	s_barrier
	ds_read_b128 v[168:171], v167 offset:16384
	ds_read_b128 v[172:175], v167 offset:17408
	ds_read_b128 v[176:179], v167 offset:18432
	ds_read_b128 v[180:183], v167 offset:19456
	ds_read_b128 v[184:187], v167 offset:20480
	ds_read_b128 v[188:191], v167 offset:21504
	ds_read_b128 v[192:195], v167 offset:22528
	ds_read_b128 v[196:199], v167 offset:23552
	global_load_lds_dwordx4 v[232:233], off
	v_lshl_add_u64 v[234:235], s[42:43], 0, v[146:147]
	s_mov_b32 m0, s77
	s_nop 0
	global_load_lds_dwordx4 v[234:235], off
	s_setprio 1
	s_barrier
	s_waitcnt lgkmcnt(0)
	v_mfma_f32_16x16x32_bf16 v[62:65], v[130:133], v[168:171], v[62:65]
	v_mfma_f32_16x16x32_bf16 v[54:57], v[154:157], v[168:171], v[54:57]
	v_mfma_f32_16x16x32_bf16 v[46:49], v[130:133], v[176:179], v[46:49]
	v_mfma_f32_16x16x32_bf16 v[38:41], v[154:157], v[176:179], v[38:41]
	v_mfma_f32_16x16x32_bf16 v[30:33], v[130:133], v[184:187], v[30:33]
	v_mfma_f32_16x16x32_bf16 v[22:25], v[154:157], v[184:187], v[22:25]
	v_mfma_f32_16x16x32_bf16 v[10:13], v[130:133], v[192:195], v[10:13]
	v_mfma_f32_16x16x32_bf16 v[2:5], v[154:157], v[192:195], v[2:5]
	v_mfma_f32_16x16x32_bf16 v[62:65], v[134:137], v[172:175], v[62:65]
	v_mfma_f32_16x16x32_bf16 v[54:57], v[158:161], v[172:175], v[54:57]
	v_mfma_f32_16x16x32_bf16 v[46:49], v[134:137], v[180:183], v[46:49]
	v_mfma_f32_16x16x32_bf16 v[38:41], v[158:161], v[180:183], v[38:41]
	v_mfma_f32_16x16x32_bf16 v[30:33], v[134:137], v[188:191], v[30:33]
	v_mfma_f32_16x16x32_bf16 v[22:25], v[158:161], v[188:191], v[22:25]
	v_mfma_f32_16x16x32_bf16 v[10:13], v[134:137], v[196:199], v[10:13]
	v_mfma_f32_16x16x32_bf16 v[2:5], v[158:161], v[196:199], v[2:5]
	s_setprio 0
	s_barrier
; #define G8_STAGE(bufoff, gbase, voff) do { _Pragma("unroll") for (int _i = 0; _i < 2; ++_i) \
;         __builtin_amdgcn_global_load_lds((const unsigned*)((const char*)(gbase) + (voff)[_i]), (LAS unsigned*)(lds + (bufoff) + ldsw + _i * 8192), 16, 0, 0); } while (0)
; #define G8_LDA(dst, b, h) do { _Pragma("unroll") for (int m = 0; m < 4; ++m) _Pragma("unroll") for (int k = 0; k < 2; ++k) dst[m][k] = *(const LAS bf16x8*)(lds + G8_SA(b, h) + aoff + m * 2048 + k * 1024); } while (0)
; #define G8_LDB(dst, b, h) do { _Pragma("unroll") for (int n = 0; n < 2; ++n) _Pragma("unroll") for (int k = 0; k < 2; ++k) dst[n][k] = *(const LAS bf16x8*)(lds + G8_SB(b, h) + boff + n * 2048 + k * 1024); } while (0)
; #define G8_MMA(ai, bj, At, Bt) do { __builtin_amdgcn_s_setprio(1); _Pragma("unroll") for (int m = 0; m < 4; ++m) _Pragma("unroll") for (int n = 0; n < 2; ++n) _Pragma("unroll") for (int k = 0; k < 2; ++k) \
;         acc[ai][bj][m][n] = __builtin_amdgcn_mfma_f32_16x16x32_bf16(Bt[n][k], At[m][k], acc[ai][bj][m][n], 0, 0, 0); __builtin_amdgcn_s_setprio(0); } while (0)
; #define G8_WAIT_V(n) asm volatile("s_waitcnt vmcnt(" #n ")" ::: "memory")
; #define G8_WAIT_L(n) asm volatile("s_waitcnt lgkmcnt(" #n ")" ::: "memory")
; #define G8_BAR __builtin_amdgcn_s_barrier()
; #define G8_SCHED __builtin_amdgcn_sched_barrier(0)
; template <class Epi, class Sched>
; __device__ __forceinline__ void gemm_phase(LAS unsigned char* lds, const int K, const Sched& S, const Epi& E) {
;     ...
;             G8_STAGE(G8_SB(0, 1), b2 + hstep, voffB);
;             G8_WAIT_V(6); G8_BAR; G8_MMA(1, 1, At, B1); G8_BAR;
;             G8_LDB(B0, 1, 0); G8_SCHED; G8_LDA(At, 1, 0); G8_STAGE(G8_SA(0, 1), a2, oc[1]);
;             G8_WAIT_L(8); G8_BAR; G8_WAIT_L(0); G8_MMA(0, 0, At, B0); G8_BAR; G8_SCHED;
;             G8_LDB(B1, 1, 1); G8_STAGE(G8_SB(1, 0), b3, voffB);
;             G8_BAR; G8_WAIT_L(0); G8_MMA(0, 1, At, B1); G8_BAR;
;             G8_LDA(At, 1, 1); G8_STAGE(G8_SA(1, 0), a3, oc[0]);
	s_add_u32 s0, s38, 0x40000
	s_addc_u32 s1, s39, 0
	s_add_i32 s49, s54, s65
	v_lshl_add_u64 v[130:131], s[0:1], 0, v[0:1]
	s_mov_b32 m0, s49
	s_nop 0
	global_load_lds_dwordx4 v[130:131], off
	v_lshl_add_u64 v[130:131], s[0:1], 0, v[140:141]
	s_add_i32 m0, s49, 0x2000
	s_nop 0
	global_load_lds_dwordx4 v[130:131], off
	s_waitcnt vmcnt(6)
	s_setprio 1
	s_barrier
	v_mfma_f32_16x16x32_bf16 v[58:61], v[216:219], v[168:171], v[58:61]
	v_mfma_f32_16x16x32_bf16 v[50:53], v[224:227], v[168:171], v[50:53]
	v_mfma_f32_16x16x32_bf16 v[42:45], v[216:219], v[176:179], v[42:45]
	v_mfma_f32_16x16x32_bf16 v[34:37], v[224:227], v[176:179], v[34:37]
	v_mfma_f32_16x16x32_bf16 v[26:29], v[216:219], v[184:187], v[26:29]
	v_mfma_f32_16x16x32_bf16 v[18:21], v[224:227], v[184:187], v[18:21]
	v_mfma_f32_16x16x32_bf16 v[14:17], v[216:219], v[192:195], v[14:17]
	v_mfma_f32_16x16x32_bf16 v[6:9], v[224:227], v[192:195], v[6:9]
	v_mfma_f32_16x16x32_bf16 v[58:61], v[220:223], v[172:175], v[58:61]
	s_add_i32 s0, 0, 0x18000
	v_mfma_f32_16x16x32_bf16 v[50:53], v[228:231], v[172:175], v[50:53]
	v_add_u32_e32 v158, s0, v165
	v_mfma_f32_16x16x32_bf16 v[42:45], v[220:223], v[180:183], v[42:45]
	v_mfma_f32_16x16x32_bf16 v[34:37], v[228:231], v[180:183], v[34:37]
	v_mfma_f32_16x16x32_bf16 v[26:29], v[220:223], v[188:191], v[26:29]
	v_mfma_f32_16x16x32_bf16 v[18:21], v[228:231], v[188:191], v[18:21]
	v_mfma_f32_16x16x32_bf16 v[14:17], v[220:223], v[196:199], v[14:17]
	v_mfma_f32_16x16x32_bf16 v[6:9], v[228:231], v[196:199], v[6:9]
	s_setprio 0
	s_barrier
	ds_read_b128 v[130:133], v158
	ds_read_b128 v[134:137], v158 offset:1024
	ds_read_b128 v[154:157], v158 offset:2048
	ds_read_b128 v[158:161], v158 offset:3072
	s_mov_b32 m0, s78
	v_lshl_add_u64 v[216:217], s[42:43], 0, v[144:145]
	ds_read_b128 v[168:171], v167 offset:32768
	ds_read_b128 v[172:175], v167 offset:33792
	ds_read_b128 v[176:179], v167 offset:34816
	ds_read_b128 v[180:183], v167 offset:35840
	ds_read_b128 v[184:187], v167 offset:36864
	ds_read_b128 v[188:191], v167 offset:37888
	ds_read_b128 v[192:195], v167 offset:38912
	ds_read_b128 v[196:199], v167 offset:39936
	global_load_lds_dwordx4 v[216:217], off
	v_lshl_add_u64 v[216:217], s[42:43], 0, v[148:149]
	s_mov_b32 m0, s79
	s_nop 0
	global_load_lds_dwordx4 v[216:217], off
	s_waitcnt lgkmcnt(8)
	s_setprio 1
	s_barrier
	s_waitcnt lgkmcnt(0)
	v_mfma_f32_16x16x32_bf16 v[126:129], v[130:133], v[168:171], v[126:129]
	v_mfma_f32_16x16x32_bf16 v[118:121], v[154:157], v[168:171], v[118:121]
	v_mfma_f32_16x16x32_bf16 v[110:113], v[130:133], v[176:179], v[110:113]
	v_mfma_f32_16x16x32_bf16 v[102:105], v[154:157], v[176:179], v[102:105]
	v_mfma_f32_16x16x32_bf16 v[94:97], v[130:133], v[184:187], v[94:97]
	v_mfma_f32_16x16x32_bf16 v[86:89], v[154:157], v[184:187], v[86:89]
	v_mfma_f32_16x16x32_bf16 v[78:81], v[130:133], v[192:195], v[78:81]
	v_mfma_f32_16x16x32_bf16 v[70:73], v[154:157], v[192:195], v[70:73]
	v_mfma_f32_16x16x32_bf16 v[126:129], v[134:137], v[172:175], v[126:129]
	v_mfma_f32_16x16x32_bf16 v[118:121], v[158:161], v[172:175], v[118:121]
	v_mfma_f32_16x16x32_bf16 v[110:113], v[134:137], v[180:183], v[110:113]
	v_mfma_f32_16x16x32_bf16 v[102:105], v[158:161], v[180:183], v[102:105]
	v_mfma_f32_16x16x32_bf16 v[94:97], v[134:137], v[188:191], v[94:97]
	v_mfma_f32_16x16x32_bf16 v[86:89], v[158:161], v[188:191], v[86:89]
	v_mfma_f32_16x16x32_bf16 v[78:81], v[134:137], v[196:199], v[78:81]
	v_mfma_f32_16x16x32_bf16 v[70:73], v[158:161], v[196:199], v[70:73]
	s_setprio 0
	s_barrier
	s_add_i32 s42, 0, 0x1c000
	s_add_i32 s0, s0, s65
	v_add_u32_e32 v213, s42, v165
	v_lshl_add_u64 v[162:163], v[162:163], 0, s[18:19]
	s_mov_b32 m0, s0
	ds_read_b128 v[216:219], v213
	ds_read_b128 v[220:223], v213 offset:1024
	ds_read_b128 v[224:227], v213 offset:2048
	ds_read_b128 v[228:231], v213 offset:3072
	global_load_lds_dwordx4 v[162:163], off
	v_lshl_add_u64 v[162:163], v[200:201], 0, s[18:19]
	s_add_i32 m0, s0, 0x2000
	s_nop 0
	global_load_lds_dwordx4 v[162:163], off
	s_setprio 1
	s_barrier
	s_waitcnt lgkmcnt(0)
	v_mfma_f32_16x16x32_bf16 v[122:125], v[216:219], v[168:171], v[122:125]
	v_mfma_f32_16x16x32_bf16 v[114:117], v[224:227], v[168:171], v[114:117]
	v_mfma_f32_16x16x32_bf16 v[106:109], v[216:219], v[176:179], v[106:109]
	v_mfma_f32_16x16x32_bf16 v[98:101], v[224:227], v[176:179], v[98:101]
	v_mfma_f32_16x16x32_bf16 v[90:93], v[216:219], v[184:187], v[90:93]
	v_mfma_f32_16x16x32_bf16 v[82:85], v[224:227], v[184:187], v[82:85]
	v_mfma_f32_16x16x32_bf16 v[74:77], v[216:219], v[192:195], v[74:77]
	v_mfma_f32_16x16x32_bf16 v[66:69], v[224:227], v[192:195], v[66:69]
	v_mfma_f32_16x16x32_bf16 v[122:125], v[220:223], v[172:175], v[122:125]
	s_mov_b32 m0, s81
	v_mfma_f32_16x16x32_bf16 v[114:117], v[228:231], v[172:175], v[114:117]
	v_lshl_add_u64 v[162:163], v[232:233], 0, s[18:19]
	v_mfma_f32_16x16x32_bf16 v[106:109], v[220:223], v[180:183], v[106:109]
	v_mfma_f32_16x16x32_bf16 v[98:101], v[228:231], v[180:183], v[98:101]
	v_mfma_f32_16x16x32_bf16 v[90:93], v[220:223], v[188:191], v[90:93]
	v_mfma_f32_16x16x32_bf16 v[82:85], v[228:231], v[188:191], v[82:85]
	v_mfma_f32_16x16x32_bf16 v[74:77], v[220:223], v[196:199], v[74:77]
	v_mfma_f32_16x16x32_bf16 v[66:69], v[228:231], v[196:199], v[66:69]
	s_setprio 0
	s_barrier
	ds_read_b128 v[168:171], v167 offset:49152
	ds_read_b128 v[172:175], v167 offset:50176
	ds_read_b128 v[176:179], v167 offset:51200
	ds_read_b128 v[180:183], v167 offset:52224
	ds_read_b128 v[184:187], v167 offset:53248
	ds_read_b128 v[188:191], v167 offset:54272
	ds_read_b128 v[192:195], v167 offset:55296
	ds_read_b128 v[196:199], v167 offset:56320
	global_load_lds_dwordx4 v[162:163], off
	v_lshl_add_u64 v[162:163], v[234:235], 0, s[18:19]
	s_mov_b32 m0, s82
	s_nop 0
	global_load_lds_dwordx4 v[162:163], off
	s_setprio 1
	s_barrier
; #define G8_WAIT_V(n) asm volatile("s_waitcnt vmcnt(" #n ")" ::: "memory")
; template <class Epi, class Sched>
; __device__ __forceinline__ void gemm_phase(LAS unsigned char* lds, const int K, const Sched& S, const Epi& E) {
;     ...
;             G8_LDA(At, 1, 1); G8_STAGE(G8_SA(1, 0), a3, oc[0]);
;             G8_BAR; G8_WAIT_L(0); G8_MMA(1, 0, At, B0); G8_BAR; G8_SCHED;
;             G8_STAGE(G8_SB(1, 1), b3 + hstep, voffB);
;             G8_WAIT_V(6); G8_BAR; G8_MMA(1, 1, At, B1); G8_BAR;
;         }
;     __device__ __forceinline__ void operator()(const f32x4 (&acc)[2][2][4][2], const g8::Unit& u, int wr, int wc, int fr_, int fq_) const {
;     ...
;         const int pn = u.pn; const int colp = pn * 256 + wc * 32 + fq * 8;
;         bf16_t* qb = (bf16_t*)(ws + AB_QB); bf16_t* kb = (bf16_t*)(ws + AB_KB); bf16_t* vT = (bf16_t*)(ws + AB_VT); bf16_t* rqb = (bf16_t*)(ws + AB_RQB); bf16_t* rkb = (bf16_t*)(ws + AB_RKB);
;         bf16_t* rkdT = (bf16_t*)(ws + AB_RKDT); bf16_t* rvT = (bf16_t*)(ws + AB_RVT); bf16_t* rgb = (bf16_t*)(ws + AB_RGB);
;         const float frqA0 = exp2f(-(float)(fq * 8) * (13.287712379549449f / 32.f)) * 0.15915494309189535f;
;         const float frqR0 = exp2f(-(float)((wc & 1) * 32 + fq * 8) * (13.287712379549449f / 63.f)) * 0.15915494309189535f;
;         constexpr float RA[8] = {1.f, 0.7498942093324559f, 0.5623413251903491f, 0.4216965034285822f, 0.31622776601683794f, 0.23713737056616552f, 0.1778279410038923f, 0.1333521432163324f};
;         constexpr float RR[8] = {1.f, 0.8639884494839686f, 0.746476040841712f, 0.6449466771037624f, 0.5572264795507174f, 0.4814372420784346f, 0.4159562163071847f, 0.35938136638046275f};
; #pragma unroll
;         for (int ai = 0; ai < 2; ++ai)
; #pragma unroll
;             for (int m = 0; m < 4; ++m) {
;                 const int t = u.pm * 256 + ai * 128 + wr * 64 + m * 16 + fr, sq = t & (SEQ - 1), b = t >> 13;
;                 f32x4 x[2][2];
; #pragma unroll
;                 for (int bj = 0; bj < 2; ++bj)
; #pragma unroll
;                     for (int n = 0; n < 2; ++n) x[bj][n] = acc[ai][bj][m][n];
;                 if (pn < 4 || (pn == 4 && wc < 2)) {
;                     const int j0 = fq * 8; const float sc = pn < 4 ? 0.125f : 1.f;
;                     u32x4 w1, w2;
; #pragma unroll
;                     for (int n = 0; n < 2; ++n) { f32x4 o1, o2;
; #pragma unroll
	s_waitcnt lgkmcnt(0)
	v_mfma_f32_16x16x32_bf16 v[62:65], v[130:133], v[168:171], v[62:65]
	v_mfma_f32_16x16x32_bf16 v[54:57], v[154:157], v[168:171], v[54:57]
	v_mfma_f32_16x16x32_bf16 v[46:49], v[130:133], v[176:179], v[46:49]
	v_mfma_f32_16x16x32_bf16 v[38:41], v[154:157], v[176:179], v[38:41]
	v_mfma_f32_16x16x32_bf16 v[30:33], v[130:133], v[184:187], v[30:33]
	v_mfma_f32_16x16x32_bf16 v[22:25], v[154:157], v[184:187], v[22:25]
	v_mfma_f32_16x16x32_bf16 v[10:13], v[130:133], v[192:195], v[10:13]
	v_mfma_f32_16x16x32_bf16 v[2:5], v[154:157], v[192:195], v[2:5]
	v_mfma_f32_16x16x32_bf16 v[62:65], v[134:137], v[172:175], v[62:65]
	v_mfma_f32_16x16x32_bf16 v[54:57], v[158:161], v[172:175], v[54:57]
	v_mfma_f32_16x16x32_bf16 v[46:49], v[134:137], v[180:183], v[46:49]
	v_mfma_f32_16x16x32_bf16 v[38:41], v[158:161], v[180:183], v[38:41]
	v_mfma_f32_16x16x32_bf16 v[30:33], v[134:137], v[188:191], v[30:33]
	v_mfma_f32_16x16x32_bf16 v[22:25], v[158:161], v[188:191], v[22:25]
	v_mfma_f32_16x16x32_bf16 v[10:13], v[134:137], v[196:199], v[10:13]
	v_mfma_f32_16x16x32_bf16 v[2:5], v[158:161], v[196:199], v[2:5]
	s_setprio 0
	s_barrier
	s_add_u32 s0, s38, 0x40080
	s_addc_u32 s1, s39, 0
	s_add_i32 s38, s42, s65
	v_lshl_add_u64 v[130:131], s[0:1], 0, v[0:1]
	s_mov_b32 m0, s38
	s_nop 0
	global_load_lds_dwordx4 v[130:131], off
	v_lshl_add_u64 v[130:131], s[0:1], 0, v[140:141]
	s_add_i32 m0, s38, 0x2000
	s_nop 0
	global_load_lds_dwordx4 v[130:131], off
	s_waitcnt vmcnt(6)
	s_setprio 1
	s_barrier
	v_mfma_f32_16x16x32_bf16 v[58:61], v[216:219], v[168:171], v[58:61]
	v_mfma_f32_16x16x32_bf16 v[50:53], v[224:227], v[168:171], v[50:53]
	v_mfma_f32_16x16x32_bf16 v[42:45], v[216:219], v[176:179], v[42:45]
	v_mfma_f32_16x16x32_bf16 v[34:37], v[224:227], v[176:179], v[34:37]
	v_mfma_f32_16x16x32_bf16 v[26:29], v[216:219], v[184:187], v[26:29]
	v_mfma_f32_16x16x32_bf16 v[18:21], v[224:227], v[184:187], v[18:21]
	v_mfma_f32_16x16x32_bf16 v[14:17], v[216:219], v[192:195], v[14:17]
	v_mfma_f32_16x16x32_bf16 v[6:9], v[224:227], v[192:195], v[6:9]
	v_mfma_f32_16x16x32_bf16 v[58:61], v[220:223], v[172:175], v[58:61]
	s_add_i32 s47, s47, 2
	v_mfma_f32_16x16x32_bf16 v[50:53], v[228:231], v[172:175], v[50:53]
	s_add_u32 s3, s3, 0x100
	v_mfma_f32_16x16x32_bf16 v[42:45], v[220:223], v[180:183], v[42:45]
	s_addc_u32 s14, s14, 0
	v_mfma_f32_16x16x32_bf16 v[34:37], v[228:231], v[180:183], v[34:37]
	s_cmp_gt_u32 s47, 13
	v_mfma_f32_16x16x32_bf16 v[26:29], v[220:223], v[188:191], v[26:29]
	s_mov_b64 s[0:1], s[12:13]
	v_mfma_f32_16x16x32_bf16 v[18:21], v[228:231], v[188:191], v[18:21]
	v_mfma_f32_16x16x32_bf16 v[14:17], v[220:223], v[196:199], v[14:17]
	v_mfma_f32_16x16x32_bf16 v[6:9], v[228:231], v[196:199], v[6:9]
	s_setprio 0
	s_barrier
	s_cbranch_scc0 .LBB0_487
	s_nop 0
	s_nop 0
	s_nop 0
	s_nop 0
	s_nop 0
	s_nop 0
	s_nop 0
	s_nop 0
	s_nop 0
	s_nop 0
	s_nop 0
	s_nop 0
	s_nop 0
	s_nop 0
	s_nop 0
	s_nop 0
	s_lshl_b32 s2, s2, 8
	s_add_i32 s2, s2, s80
	s_cmp_lt_i32 s94, 4
	s_cselect_b64 s[36:37], -1, 0
	s_cmp_lg_u32 s94, 4
	v_mov_b32_e32 v131, v164
	v_mov_b32_e32 v130, v139
	s_cselect_b64 s[12:13], -1, 0
	s_cmp_eq_u32 s94, 4
	s_nop 0
	v_add_u32_e32 v160, s2, v131
	s_cselect_b64 s[2:3], -1, 0
	s_and_b64 s[2:3], s[2:3], s[10:11]
	s_cmp_gt_u32 s94, 8
	s_cselect_b64 s[56:57], -1, 0
	s_cmp_gt_u32 s94, 12
	s_cselect_b64 s[54:55], -1, 0
	s_lshl_b32 s42, s94, 8
	s_add_i32 s14, s42, 0xfffff300
	v_lshlrev_b32_e32 v130, 3, v130
	s_lshl_b64 s[22:23], s[14:15], 1
	v_add_u32_e32 v132, s85, v130
	s_add_u32 s22, s87, s22
	v_cvt_f32_i32_e32 v133, v132
	s_addc_u32 s23, s88, s23
	s_add_i32 s14, s86, s42
	s_cmp_gt_u32 s94, 6
	v_add_u32_e32 v171, s14, v130
	s_cselect_b64 s[38:39], -1, 0
	s_lshl_b32 s14, s94, 1
	s_and_b32 s14, s14, 2
	v_mul_f32_e32 v134, 0xbe57fa62, v133
	s_or_b32 s14, s14, s89
	v_cmp_gt_f32_e32 vcc, s66, v134
	v_ashrrev_i32_e32 v131, 31, v130
	s_lshl_b32 s14, s14, 7
	v_cvt_f32_i32_e32 v172, v130
	v_cndmask_b32_e32 v134, 0, v207, vcc
	v_lshlrev_b64 v[162:163], 1, v[130:131]
	s_xor_b32 s14, s14, 0x100
	v_fmac_f32_e32 v134, 0xbe57fa62, v133
	v_lshl_add_u64 v[158:159], s[22:23], 0, v[162:163]
	s_and_b64 s[22:23], s[38:39], exec
	v_exp_f32_e32 v133, v134
	s_mov_b32 s22, 0x3d420000
	s_cselect_b32 s22, s22, 0x3c420000
	v_mul_f32_e32 v134, 0xbed49a78, v172
	s_add_u32 s22, s40, s22
	v_cmp_gt_f32_e64 s[0:1], s66, v134
	v_cndmask_b32_e32 v134, 0, v208, vcc
	v_add_u32_e32 v170, s14, v132
	s_addc_u32 s23, s41, 0
	s_lshl_b32 s14, s14, 1
	v_ldexp_f32 v133, v133, v134
	s_add_u32 s22, s22, s14
	v_mul_f32_e32 v169, 0.15915494, v133
	s_addc_u32 s23, s23, 0
	v_ashrrev_i32_e32 v133, 31, v132
	v_lshl_add_u64 v[154:155], v[132:133], 1, s[22:23]
	s_or_b32 s22, s42, s75
	s_ashr_i32 s23, s22, 31
	s_lshl_b64 s[22:23], s[22:23], 1
	s_add_u32 s42, s83, s22
	v_mov_b32_e32 v131, 0x3db504f3
	s_addc_u32 s43, s84, s23
	s_nor_b64 s[22:23], s[36:37], s[2:3]
	v_cndmask_b32_e64 v156, 1.0, v131, s[38:39]
	v_add_u32_e32 v168, s90, v130
	v_and_b32_e32 v173, 0x1fff, v160
	s_mov_b64 s[2:3], -1
	s_and_b64 vcc, exec, s[22:23]
	s_cbranch_vccz .LBB0_506
; __device__ __forceinline__ unsigned pk2(float lo, float hi) { unsigned r; asm("v_cvt_pk_bf16_f32 %0, %1, %2" : "=v"(r) : "v"(lo), "v"(hi)); return r; }
; __device__ __forceinline__ f32x4 silu4(const f32x4 x) { const f32x4 t = x * (-1.4426950408889634f); f32x4 d;
; #pragma unroll
;     for (int e = 0; e < 4; ++e) d[e] = __builtin_amdgcn_exp2f(t[e]);
;     d = d + 1.f;
; #pragma unroll
;     for (int e = 0; e < 4; ++e) d[e] = __builtin_amdgcn_rcpf(d[e]);
;     return x * d; }
;     __device__ __forceinline__ void operator()(const f32x4 (&acc)[2][2][4][2], const g8::Unit& u, int wr, int wc, int fr_, int fq_) const {
;     ...
;                 } else {
; #pragma unroll
;                     for (int bj = 0; bj < 2; ++bj) { u32x4 w;
; #pragma unroll
;                         for (int n = 0; n < 2; ++n) { const f32x4 sv = silu4(x[bj][n]); w[2 * n] = pk2(sv[0], sv[1]); w[2 * n + 1] = pk2(sv[2], sv[3]); }
;                         *(u32x4*)(rgb + (size_t)t * 1024 + (pn - 13) * 256 + bj * 128 + wc * 32 + fq * 8) = w; }
	v_ashrrev_i32_e32 v174, 13, v160
	s_and_b64 vcc, exec, s[12:13]
	s_cbranch_vccz .LBB0_503
	s_and_b64 vcc, exec, s[56:57]
	s_cbranch_vccz .LBB0_496
	s_andn2_b64 vcc, exec, s[54:55]
	s_cbranch_vccnz .LBB0_493
	v_mul_f32_e32 v132, 0xbfb8aa3b, v126
	v_mul_f32_e32 v133, 0xbfb8aa3b, v127
	v_mul_f32_e32 v134, 0xbfb8aa3b, v128
	v_mul_f32_e32 v135, 0xbfb8aa3b, v129
	v_exp_f32_e32 v132, v132
	v_exp_f32_e32 v133, v133
	v_exp_f32_e32 v134, v134
	v_exp_f32_e32 v135, v135
	v_mul_f32_e32 v136, 0xbfb8aa3b, v120
	v_pk_add_f32 v[132:133], v[132:133], 1.0 op_sel_hi:[1,0]
	v_mul_f32_e32 v137, 0xbfb8aa3b, v121
	v_pk_add_f32 v[134:135], v[134:135], 1.0 op_sel_hi:[1,0]
	v_rcp_f32_e32 v132, v132
	v_rcp_f32_e32 v133, v133
	v_rcp_f32_e32 v134, v134
	v_rcp_f32_e32 v135, v135
	v_exp_f32_e32 v136, v136
	v_pk_mul_f32 v[132:133], v[126:127], v[132:133]
	v_exp_f32_e32 v137, v137
	v_pk_mul_f32 v[134:135], v[128:129], v[134:135]
	v_cvt_pk_bf16_f32 v132, v132, v133
	v_ashrrev_i32_e32 v161, 31, v160
	v_cvt_pk_bf16_f32 v133, v134, v135
	v_mul_f32_e32 v134, 0xbfb8aa3b, v118
	v_mul_f32_e32 v135, 0xbfb8aa3b, v119
	v_exp_f32_e32 v134, v134
	v_exp_f32_e32 v135, v135
	v_pk_add_f32 v[136:137], v[136:137], 1.0 op_sel_hi:[1,0]
	v_lshlrev_b64 v[130:131], 11, v[160:161]
	v_rcp_f32_e32 v136, v136
	v_pk_add_f32 v[134:135], v[134:135], 1.0 op_sel_hi:[1,0]
	v_rcp_f32_e32 v137, v137
	v_rcp_f32_e32 v134, v134
	v_rcp_f32_e32 v135, v135
	v_lshl_add_u64 v[130:131], v[158:159], 0, v[130:131]
	v_pk_mul_f32 v[136:137], v[120:121], v[136:137]
	s_mov_b64 s[2:3], 0
	v_pk_mul_f32 v[134:135], v[118:119], v[134:135]
	s_nop 0
	v_cvt_pk_bf16_f32 v134, v134, v135
	v_cvt_pk_bf16_f32 v135, v136, v137
	global_store_dwordx4 v[130:131], v[132:135], off
	v_mul_f32_e32 v136, 0xbfb8aa3b, v116
	v_mul_f32_e32 v137, 0xbfb8aa3b, v117
	v_mul_f32_e32 v132, 0xbfb8aa3b, v122
	v_mul_f32_e32 v133, 0xbfb8aa3b, v123
	v_mul_f32_e32 v134, 0xbfb8aa3b, v124
	v_mul_f32_e32 v135, 0xbfb8aa3b, v125
	v_exp_f32_e32 v132, v132
	v_exp_f32_e32 v133, v133
	v_exp_f32_e32 v134, v134
	v_exp_f32_e32 v135, v135
	v_exp_f32_e32 v136, v136
	v_pk_add_f32 v[132:133], v[132:133], 1.0 op_sel_hi:[1,0]
	v_exp_f32_e32 v137, v137
	v_pk_add_f32 v[134:135], v[134:135], 1.0 op_sel_hi:[1,0]
	v_rcp_f32_e32 v132, v132
	v_rcp_f32_e32 v133, v133
	v_rcp_f32_e32 v134, v134
	v_rcp_f32_e32 v135, v135
	v_pk_add_f32 v[136:137], v[136:137], 1.0 op_sel_hi:[1,0]
	v_pk_mul_f32 v[132:133], v[122:123], v[132:133]
	v_rcp_f32_e32 v136, v136
	v_pk_mul_f32 v[134:135], v[124:125], v[134:135]
	v_cvt_pk_bf16_f32 v132, v132, v133
	v_rcp_f32_e32 v137, v137
	v_cvt_pk_bf16_f32 v133, v134, v135
	v_mul_f32_e32 v134, 0xbfb8aa3b, v114
	v_mul_f32_e32 v135, 0xbfb8aa3b, v115
	v_exp_f32_e32 v134, v134
	v_exp_f32_e32 v135, v135
	v_pk_mul_f32 v[136:137], v[116:117], v[136:137]
	v_pk_add_f32 v[134:135], v[134:135], 1.0 op_sel_hi:[1,0]
	s_nop 0
	v_rcp_f32_e32 v134, v134
	v_rcp_f32_e32 v135, v135
	s_nop 0
	v_pk_mul_f32 v[134:135], v[114:115], v[134:135]
	s_nop 0
	v_cvt_pk_bf16_f32 v134, v134, v135
	v_cvt_pk_bf16_f32 v135, v136, v137
	global_store_dwordx4 v[130:131], v[132:135], off offset:256

; #define G8_STAGE(bufoff, gbase, voff) do { _Pragma("unroll") for (int _i = 0; _i < 2; ++_i) \
;         __builtin_amdgcn_global_load_lds((const unsigned*)((const char*)(gbase) + (voff)[_i]), (LAS unsigned*)(lds + (bufoff) + ldsw + _i * 8192), 16, 0, 0); } while (0)
; #define G8_LDA(dst, b, h) do { _Pragma("unroll") for (int m = 0; m < 4; ++m) _Pragma("unroll") for (int k = 0; k < 2; ++k) dst[m][k] = *(const LAS bf16x8*)(lds + G8_SA(b, h) + aoff + m * 2048 + k * 1024); } while (0)
; #define G8_LDB(dst, b, h) do { _Pragma("unroll") for (int n = 0; n < 2; ++n) _Pragma("unroll") for (int k = 0; k < 2; ++k) dst[n][k] = *(const LAS bf16x8*)(lds + G8_SB(b, h) + boff + n * 2048 + k * 1024); } while (0)
; #define G8_MMA(ai, bj, At, Bt) do { __builtin_amdgcn_s_setprio(1); _Pragma("unroll") for (int m = 0; m < 4; ++m) _Pragma("unroll") for (int n = 0; n < 2; ++n) _Pragma("unroll") for (int k = 0; k < 2; ++k) \
;         acc[ai][bj][m][n] = __builtin_amdgcn_mfma_f32_16x16x32_bf16(Bt[n][k], At[m][k], acc[ai][bj][m][n], 0, 0, 0); __builtin_amdgcn_s_setprio(0); } while (0)
; #define G8_WAIT_L(n) asm volatile("s_waitcnt lgkmcnt(" #n ")" ::: "memory")
; #define G8_BAR __builtin_amdgcn_s_barrier()
; #define G8_SCHED __builtin_amdgcn_sched_barrier(0)
; template <class Epi, class Sched>
; __device__ __forceinline__ void gemm_phase(LAS unsigned char* lds, const int K, const Sched& S, const Epi& E) {
;     ...
;             const bool last = (t == nt - 2);
;             const char* a1 = cA + (size_t)(t + 1) * kstep;
;             const char* a2 = last ? nA : cA + (size_t)(t + 2) * kstep; const char* b2 = last ? nB : cB + (size_t)(t + 2) * kstep;
;             const char* a3 = a2 + kstep; const char* b3 = b2 + kstep;
;             G8_LDB(B0, 0, 0); G8_SCHED; G8_LDA(At, 0, 0); G8_STAGE(G8_SA(1, 1), a1, oc[1]);
;             if (last && has_next) S.aoff(nxt, tid, oc);
;             G8_WAIT_L(8); G8_BAR; G8_WAIT_L(0); G8_MMA(0, 0, At, B0); G8_BAR; G8_SCHED;
;             G8_LDB(B1, 0, 1); G8_STAGE(G8_SB(0, 0), b2, voffB);
;             G8_BAR; G8_WAIT_L(0); G8_MMA(0, 1, At, B1); G8_BAR;
;             G8_LDA(At, 0, 1); G8_STAGE(G8_SA(0, 0), a2, oc[0]);
;             G8_BAR; G8_WAIT_L(0); G8_MMA(1, 0, At, B0); G8_BAR; G8_SCHED;
.LBB0_2252:
	s_add_i32 s60, s22, 2
	s_add_u32 s24, s12, 0x80
	s_addc_u32 s23, s13, 0
	s_add_i32 s61, 0, 0x10000
	v_add_u32_e32 v144, s61, v148
	ds_read_b128 v[152:155], v144
	ds_read_b128 v[156:159], v144 offset:1024
	ds_read_b128 v[160:163], v144 offset:2048
	ds_read_b128 v[164:167], v144 offset:3072
	s_cmp_eq_u32 s51, s22
	s_cselect_b32 s22, s0, s24
	s_cselect_b32 s23, s1, s23
	s_cselect_b32 s25, s11, s59
	s_cselect_b32 s24, s10, s58
	v_lshl_add_u64 v[144:145], s[12:13], 0, v[140:141]
	s_add_i32 m0, s44, 0xc000
	ds_read_b128 v[168:171], v150
	ds_read_b128 v[172:175], v150 offset:1024
	ds_read_b128 v[176:179], v150 offset:2048
	ds_read_b128 v[180:183], v150 offset:3072
	ds_read_b128 v[184:187], v150 offset:4096
	ds_read_b128 v[188:191], v150 offset:5120
	ds_read_b128 v[192:195], v150 offset:6144
	ds_read_b128 v[196:199], v150 offset:7168
	global_load_lds_dwordx4 v[144:145], off
	v_lshl_add_u64 v[144:145], s[12:13], 0, v[142:143]
	s_add_i32 m0, s44, 0xe000
	s_nop 0
	global_load_lds_dwordx4 v[144:145], off
	s_waitcnt lgkmcnt(8)
	s_setprio 1
	s_barrier
	s_waitcnt lgkmcnt(0)
	v_mfma_f32_16x16x32_bf16 v[126:129], v[152:155], v[168:171], v[126:129]
	v_mfma_f32_16x16x32_bf16 v[122:125], v[160:163], v[168:171], v[122:125]
	v_mfma_f32_16x16x32_bf16 v[110:113], v[152:155], v[176:179], v[110:113]
	v_mfma_f32_16x16x32_bf16 v[106:109], v[160:163], v[176:179], v[106:109]
	v_mfma_f32_16x16x32_bf16 v[94:97], v[152:155], v[184:187], v[94:97]
	v_mfma_f32_16x16x32_bf16 v[90:93], v[160:163], v[184:187], v[90:93]
	v_mfma_f32_16x16x32_bf16 v[78:81], v[152:155], v[192:195], v[78:81]
	v_mfma_f32_16x16x32_bf16 v[74:77], v[160:163], v[192:195], v[74:77]
	v_mfma_f32_16x16x32_bf16 v[126:129], v[156:159], v[172:175], v[126:129]
	v_mfma_f32_16x16x32_bf16 v[122:125], v[164:167], v[172:175], v[122:125]
	v_mfma_f32_16x16x32_bf16 v[110:113], v[156:159], v[180:183], v[110:113]
	v_mfma_f32_16x16x32_bf16 v[106:109], v[164:167], v[180:183], v[106:109]
	v_mfma_f32_16x16x32_bf16 v[94:97], v[156:159], v[188:191], v[94:97]
	v_mfma_f32_16x16x32_bf16 v[90:93], v[164:167], v[188:191], v[90:93]
	v_mfma_f32_16x16x32_bf16 v[78:81], v[156:159], v[196:199], v[78:81]
	v_mfma_f32_16x16x32_bf16 v[74:77], v[164:167], v[196:199], v[74:77]
	s_setprio 0
	s_barrier
	s_add_i32 s62, 0, 0x14000
	v_add_u32_e32 v144, s62, v148
	s_add_i32 s61, s61, s43
	ds_read_b128 v[216:219], v144
	ds_read_b128 v[220:223], v144 offset:1024
	ds_read_b128 v[224:227], v144 offset:2048
	ds_read_b128 v[228:231], v144 offset:3072
	v_lshl_add_u64 v[144:145], s[24:25], 0, v[0:1]
	s_mov_b32 m0, s61
	v_lshl_add_u64 v[200:201], s[24:25], 0, v[130:131]
	global_load_lds_dwordx4 v[144:145], off
	s_add_i32 m0, s61, 0x2000
	s_nop 0
	global_load_lds_dwordx4 v[200:201], off
	s_setprio 1
	s_barrier
	s_waitcnt lgkmcnt(0)
	v_mfma_f32_16x16x32_bf16 v[118:121], v[216:219], v[168:171], v[118:121]
	v_mfma_f32_16x16x32_bf16 v[114:117], v[224:227], v[168:171], v[114:117]
	v_mfma_f32_16x16x32_bf16 v[102:105], v[216:219], v[176:179], v[102:105]
	v_mfma_f32_16x16x32_bf16 v[98:101], v[224:227], v[176:179], v[98:101]
	v_mfma_f32_16x16x32_bf16 v[86:89], v[216:219], v[184:187], v[86:89]
	v_mfma_f32_16x16x32_bf16 v[82:85], v[224:227], v[184:187], v[82:85]
	v_mfma_f32_16x16x32_bf16 v[70:73], v[216:219], v[192:195], v[70:73]
	v_mfma_f32_16x16x32_bf16 v[66:69], v[224:227], v[192:195], v[66:69]
	v_mfma_f32_16x16x32_bf16 v[118:121], v[220:223], v[172:175], v[118:121]
	s_mov_b32 m0, s44
	v_mfma_f32_16x16x32_bf16 v[114:117], v[228:231], v[172:175], v[114:117]
	v_lshl_add_u64 v[232:233], s[22:23], 0, v[132:133]
	v_mfma_f32_16x16x32_bf16 v[102:105], v[220:223], v[180:183], v[102:105]
	v_mfma_f32_16x16x32_bf16 v[98:101], v[228:231], v[180:183], v[98:101]
	v_mfma_f32_16x16x32_bf16 v[86:89], v[220:223], v[188:191], v[86:89]
	v_mfma_f32_16x16x32_bf16 v[82:85], v[228:231], v[188:191], v[82:85]
	v_mfma_f32_16x16x32_bf16 v[70:73], v[220:223], v[196:199], v[70:73]
	v_mfma_f32_16x16x32_bf16 v[66:69], v[228:231], v[196:199], v[66:69]
	s_setprio 0
	s_barrier
	ds_read_b128 v[168:171], v150 offset:16384
	ds_read_b128 v[172:175], v150 offset:17408
	ds_read_b128 v[176:179], v150 offset:18432
	ds_read_b128 v[180:183], v150 offset:19456
	ds_read_b128 v[184:187], v150 offset:20480
	ds_read_b128 v[188:191], v150 offset:21504
	ds_read_b128 v[192:195], v150 offset:22528
	ds_read_b128 v[196:199], v150 offset:23552
	global_load_lds_dwordx4 v[232:233], off
	v_lshl_add_u64 v[234:235], s[22:23], 0, v[136:137]
	s_mov_b32 m0, s45
	s_nop 0
	global_load_lds_dwordx4 v[234:235], off
	s_setprio 1
	s_barrier
	s_waitcnt lgkmcnt(0)
	v_mfma_f32_16x16x32_bf16 v[62:65], v[152:155], v[168:171], v[62:65]
	v_mfma_f32_16x16x32_bf16 v[58:61], v[160:163], v[168:171], v[58:61]
	v_mfma_f32_16x16x32_bf16 v[46:49], v[152:155], v[176:179], v[46:49]
	v_mfma_f32_16x16x32_bf16 v[42:45], v[160:163], v[176:179], v[42:45]
	v_mfma_f32_16x16x32_bf16 v[30:33], v[152:155], v[184:187], v[30:33]
	v_mfma_f32_16x16x32_bf16 v[26:29], v[160:163], v[184:187], v[26:29]
	v_mfma_f32_16x16x32_bf16 v[14:17], v[152:155], v[192:195], v[14:17]
	v_mfma_f32_16x16x32_bf16 v[10:13], v[160:163], v[192:195], v[10:13]
	v_mfma_f32_16x16x32_bf16 v[62:65], v[156:159], v[172:175], v[62:65]
	v_mfma_f32_16x16x32_bf16 v[58:61], v[164:167], v[172:175], v[58:61]
	v_mfma_f32_16x16x32_bf16 v[46:49], v[156:159], v[180:183], v[46:49]
	v_mfma_f32_16x16x32_bf16 v[42:45], v[164:167], v[180:183], v[42:45]
	v_mfma_f32_16x16x32_bf16 v[30:33], v[156:159], v[188:191], v[30:33]
	v_mfma_f32_16x16x32_bf16 v[26:29], v[164:167], v[188:191], v[26:29]
	v_mfma_f32_16x16x32_bf16 v[14:17], v[156:159], v[196:199], v[14:17]
	v_mfma_f32_16x16x32_bf16 v[10:13], v[164:167], v[196:199], v[10:13]
	s_setprio 0
	s_barrier
; #define G8_STAGE(bufoff, gbase, voff) do { _Pragma("unroll") for (int _i = 0; _i < 2; ++_i) \
;         __builtin_amdgcn_global_load_lds((const unsigned*)((const char*)(gbase) + (voff)[_i]), (LAS unsigned*)(lds + (bufoff) + ldsw + _i * 8192), 16, 0, 0); } while (0)
; #define G8_LDA(dst, b, h) do { _Pragma("unroll") for (int m = 0; m < 4; ++m) _Pragma("unroll") for (int k = 0; k < 2; ++k) dst[m][k] = *(const LAS bf16x8*)(lds + G8_SA(b, h) + aoff + m * 2048 + k * 1024); } while (0)
; #define G8_LDB(dst, b, h) do { _Pragma("unroll") for (int n = 0; n < 2; ++n) _Pragma("unroll") for (int k = 0; k < 2; ++k) dst[n][k] = *(const LAS bf16x8*)(lds + G8_SB(b, h) + boff + n * 2048 + k * 1024); } while (0)
; #define G8_MMA(ai, bj, At, Bt) do { __builtin_amdgcn_s_setprio(1); _Pragma("unroll") for (int m = 0; m < 4; ++m) _Pragma("unroll") for (int n = 0; n < 2; ++n) _Pragma("unroll") for (int k = 0; k < 2; ++k) \
;         acc[ai][bj][m][n] = __builtin_amdgcn_mfma_f32_16x16x32_bf16(Bt[n][k], At[m][k], acc[ai][bj][m][n], 0, 0, 0); __builtin_amdgcn_s_setprio(0); } while (0)
; #define G8_WAIT_V(n) asm volatile("s_waitcnt vmcnt(" #n ")" ::: "memory")
; #define G8_WAIT_L(n) asm volatile("s_waitcnt lgkmcnt(" #n ")" ::: "memory")
; #define G8_BAR __builtin_amdgcn_s_barrier()
; #define G8_SCHED __builtin_amdgcn_sched_barrier(0)
; template <class Epi, class Sched>
; __device__ __forceinline__ void gemm_phase(LAS unsigned char* lds, const int K, const Sched& S, const Epi& E) {
;     ...
;             G8_STAGE(G8_SB(0, 1), b2 + hstep, voffB);
;             G8_WAIT_V(6); G8_BAR; G8_MMA(1, 1, At, B1); G8_BAR;
;             G8_LDB(B0, 1, 0); G8_SCHED; G8_LDA(At, 1, 0); G8_STAGE(G8_SA(0, 1), a2, oc[1]);
;             G8_WAIT_L(8); G8_BAR; G8_WAIT_L(0); G8_MMA(0, 0, At, B0); G8_BAR; G8_SCHED;
;             G8_LDB(B1, 1, 1); G8_STAGE(G8_SB(1, 0), b3, voffB);
;             G8_BAR; G8_WAIT_L(0); G8_MMA(0, 1, At, B1); G8_BAR;
;             G8_LDA(At, 1, 1); G8_STAGE(G8_SA(1, 0), a3, oc[0]);
	s_add_u32 s24, s24, s42
	s_addc_u32 s25, s25, 0
	s_add_i32 s61, s62, s43
	v_lshl_add_u64 v[236:237], s[24:25], 0, v[0:1]
	s_mov_b32 m0, s61
	v_lshl_add_u64 v[238:239], s[24:25], 0, v[130:131]
	global_load_lds_dwordx4 v[236:237], off
	s_add_i32 m0, s61, 0x2000
	s_nop 0
	global_load_lds_dwordx4 v[238:239], off
	s_waitcnt vmcnt(6)
	s_setprio 1
	s_barrier
	v_mfma_f32_16x16x32_bf16 v[54:57], v[216:219], v[168:171], v[54:57]
	v_mfma_f32_16x16x32_bf16 v[50:53], v[224:227], v[168:171], v[50:53]
	v_mfma_f32_16x16x32_bf16 v[38:41], v[216:219], v[176:179], v[38:41]
	v_mfma_f32_16x16x32_bf16 v[34:37], v[224:227], v[176:179], v[34:37]
	v_mfma_f32_16x16x32_bf16 v[22:25], v[216:219], v[184:187], v[22:25]
	v_mfma_f32_16x16x32_bf16 v[18:21], v[224:227], v[184:187], v[18:21]
	v_mfma_f32_16x16x32_bf16 v[6:9], v[216:219], v[192:195], v[6:9]
	v_mfma_f32_16x16x32_bf16 v[2:5], v[224:227], v[192:195], v[2:5]
	v_mfma_f32_16x16x32_bf16 v[54:57], v[220:223], v[172:175], v[54:57]
	s_add_i32 s24, 0, 0x18000
	v_mfma_f32_16x16x32_bf16 v[50:53], v[228:231], v[172:175], v[50:53]
	v_add_u32_e32 v151, s24, v148
	v_mfma_f32_16x16x32_bf16 v[38:41], v[220:223], v[180:183], v[38:41]
	v_mfma_f32_16x16x32_bf16 v[34:37], v[228:231], v[180:183], v[34:37]
	v_mfma_f32_16x16x32_bf16 v[22:25], v[220:223], v[188:191], v[22:25]
	v_mfma_f32_16x16x32_bf16 v[18:21], v[228:231], v[188:191], v[18:21]
	v_mfma_f32_16x16x32_bf16 v[6:9], v[220:223], v[196:199], v[6:9]
	v_mfma_f32_16x16x32_bf16 v[2:5], v[228:231], v[196:199], v[2:5]
	s_setprio 0
	s_barrier
	ds_read_b128 v[152:155], v151
	ds_read_b128 v[156:159], v151 offset:1024
	ds_read_b128 v[160:163], v151 offset:2048
	ds_read_b128 v[164:167], v151 offset:3072
	s_mov_b32 m0, s46
	v_lshl_add_u64 v[216:217], s[22:23], 0, v[134:135]
	ds_read_b128 v[168:171], v150 offset:32768
	ds_read_b128 v[172:175], v150 offset:33792
	ds_read_b128 v[176:179], v150 offset:34816
	ds_read_b128 v[180:183], v150 offset:35840
	ds_read_b128 v[184:187], v150 offset:36864
	ds_read_b128 v[188:191], v150 offset:37888
	ds_read_b128 v[192:195], v150 offset:38912
	ds_read_b128 v[196:199], v150 offset:39936
	global_load_lds_dwordx4 v[216:217], off
	v_lshl_add_u64 v[216:217], s[22:23], 0, v[138:139]
	s_mov_b32 m0, s47
	s_nop 0
	global_load_lds_dwordx4 v[216:217], off
	s_waitcnt lgkmcnt(8)
	s_setprio 1
	s_barrier
	s_waitcnt lgkmcnt(0)
	v_mfma_f32_16x16x32_bf16 v[126:129], v[152:155], v[168:171], v[126:129]
	v_mfma_f32_16x16x32_bf16 v[122:125], v[160:163], v[168:171], v[122:125]
	v_mfma_f32_16x16x32_bf16 v[110:113], v[152:155], v[176:179], v[110:113]
	v_mfma_f32_16x16x32_bf16 v[106:109], v[160:163], v[176:179], v[106:109]
	v_mfma_f32_16x16x32_bf16 v[94:97], v[152:155], v[184:187], v[94:97]
	v_mfma_f32_16x16x32_bf16 v[90:93], v[160:163], v[184:187], v[90:93]
	v_mfma_f32_16x16x32_bf16 v[78:81], v[152:155], v[192:195], v[78:81]
	v_mfma_f32_16x16x32_bf16 v[74:77], v[160:163], v[192:195], v[74:77]
	v_mfma_f32_16x16x32_bf16 v[126:129], v[156:159], v[172:175], v[126:129]
	v_mfma_f32_16x16x32_bf16 v[122:125], v[164:167], v[172:175], v[122:125]
	v_mfma_f32_16x16x32_bf16 v[110:113], v[156:159], v[180:183], v[110:113]
	v_mfma_f32_16x16x32_bf16 v[106:109], v[164:167], v[180:183], v[106:109]
	v_mfma_f32_16x16x32_bf16 v[94:97], v[156:159], v[188:191], v[94:97]
	v_mfma_f32_16x16x32_bf16 v[90:93], v[164:167], v[188:191], v[90:93]
	v_mfma_f32_16x16x32_bf16 v[78:81], v[156:159], v[196:199], v[78:81]
	v_mfma_f32_16x16x32_bf16 v[74:77], v[164:167], v[196:199], v[74:77]
	s_setprio 0
	s_barrier
	s_add_i32 s22, 0, 0x1c000
	s_add_i32 s23, s24, s43
	v_add_u32_e32 v151, s22, v148
	v_lshl_add_u64 v[144:145], v[144:145], 0, s[18:19]
	s_mov_b32 m0, s23
	ds_read_b128 v[216:219], v151
	ds_read_b128 v[220:223], v151 offset:1024
	ds_read_b128 v[224:227], v151 offset:2048
	ds_read_b128 v[228:231], v151 offset:3072
	global_load_lds_dwordx4 v[144:145], off
	v_lshl_add_u64 v[144:145], v[200:201], 0, s[18:19]
	s_add_i32 m0, s23, 0x2000
	s_nop 0
	global_load_lds_dwordx4 v[144:145], off
	s_setprio 1
	s_barrier
	s_waitcnt lgkmcnt(0)
	v_mfma_f32_16x16x32_bf16 v[118:121], v[216:219], v[168:171], v[118:121]
	v_mfma_f32_16x16x32_bf16 v[114:117], v[224:227], v[168:171], v[114:117]
	v_mfma_f32_16x16x32_bf16 v[102:105], v[216:219], v[176:179], v[102:105]
	v_mfma_f32_16x16x32_bf16 v[98:101], v[224:227], v[176:179], v[98:101]
	v_mfma_f32_16x16x32_bf16 v[86:89], v[216:219], v[184:187], v[86:89]
	v_mfma_f32_16x16x32_bf16 v[82:85], v[224:227], v[184:187], v[82:85]
	v_mfma_f32_16x16x32_bf16 v[70:73], v[216:219], v[192:195], v[70:73]
	v_mfma_f32_16x16x32_bf16 v[66:69], v[224:227], v[192:195], v[66:69]
	v_mfma_f32_16x16x32_bf16 v[118:121], v[220:223], v[172:175], v[118:121]
	s_mov_b32 m0, s48
	v_mfma_f32_16x16x32_bf16 v[114:117], v[228:231], v[172:175], v[114:117]
	v_lshl_add_u64 v[144:145], v[232:233], 0, s[18:19]
	v_mfma_f32_16x16x32_bf16 v[102:105], v[220:223], v[180:183], v[102:105]
	v_mfma_f32_16x16x32_bf16 v[98:101], v[228:231], v[180:183], v[98:101]
	v_mfma_f32_16x16x32_bf16 v[86:89], v[220:223], v[188:191], v[86:89]
	v_mfma_f32_16x16x32_bf16 v[82:85], v[228:231], v[188:191], v[82:85]
	v_mfma_f32_16x16x32_bf16 v[70:73], v[220:223], v[196:199], v[70:73]
	v_mfma_f32_16x16x32_bf16 v[66:69], v[228:231], v[196:199], v[66:69]
	s_setprio 0
	s_barrier
	ds_read_b128 v[168:171], v150 offset:49152
	ds_read_b128 v[172:175], v150 offset:50176
	ds_read_b128 v[176:179], v150 offset:51200
	ds_read_b128 v[180:183], v150 offset:52224
	ds_read_b128 v[184:187], v150 offset:53248
	ds_read_b128 v[188:191], v150 offset:54272
	ds_read_b128 v[192:195], v150 offset:55296
	ds_read_b128 v[196:199], v150 offset:56320
	global_load_lds_dwordx4 v[144:145], off
	v_lshl_add_u64 v[144:145], v[234:235], 0, s[18:19]
	s_mov_b32 m0, s49
	s_nop 0
	global_load_lds_dwordx4 v[144:145], off
	s_setprio 1
	s_barrier
; #define G8_STAGE(bufoff, gbase, voff) do { _Pragma("unroll") for (int _i = 0; _i < 2; ++_i) \
;         __builtin_amdgcn_global_load_lds((const unsigned*)((const char*)(gbase) + (voff)[_i]), (LAS unsigned*)(lds + (bufoff) + ldsw + _i * 8192), 16, 0, 0); } while (0)
; #define G8_MMA(ai, bj, At, Bt) do { __builtin_amdgcn_s_setprio(1); _Pragma("unroll") for (int m = 0; m < 4; ++m) _Pragma("unroll") for (int n = 0; n < 2; ++n) _Pragma("unroll") for (int k = 0; k < 2; ++k) \
;         acc[ai][bj][m][n] = __builtin_amdgcn_mfma_f32_16x16x32_bf16(Bt[n][k], At[m][k], acc[ai][bj][m][n], 0, 0, 0); __builtin_amdgcn_s_setprio(0); } while (0)
; #define G8_WAIT_V(n) asm volatile("s_waitcnt vmcnt(" #n ")" ::: "memory")
; #define G8_WAIT_L(n) asm volatile("s_waitcnt lgkmcnt(" #n ")" ::: "memory")
; #define G8_BAR __builtin_amdgcn_s_barrier()
; #define G8_SCHED __builtin_amdgcn_sched_barrier(0)
; template <class Epi, class Sched>
; __device__ __forceinline__ void gemm_phase(LAS unsigned char* lds, const int K, const Sched& S, const Epi& E) {
;     ...
;             G8_BAR; G8_WAIT_L(0); G8_MMA(1, 0, At, B0); G8_BAR; G8_SCHED;
;             G8_STAGE(G8_SB(1, 1), b3 + hstep, voffB);
;             G8_WAIT_V(6); G8_BAR; G8_MMA(1, 1, At, B1); G8_BAR;
	s_waitcnt lgkmcnt(0)
	v_mfma_f32_16x16x32_bf16 v[62:65], v[152:155], v[168:171], v[62:65]
	v_mfma_f32_16x16x32_bf16 v[58:61], v[160:163], v[168:171], v[58:61]
	v_mfma_f32_16x16x32_bf16 v[46:49], v[152:155], v[176:179], v[46:49]
	v_mfma_f32_16x16x32_bf16 v[42:45], v[160:163], v[176:179], v[42:45]
	v_mfma_f32_16x16x32_bf16 v[30:33], v[152:155], v[184:187], v[30:33]
	v_mfma_f32_16x16x32_bf16 v[26:29], v[160:163], v[184:187], v[26:29]
	v_mfma_f32_16x16x32_bf16 v[14:17], v[152:155], v[192:195], v[14:17]
	v_mfma_f32_16x16x32_bf16 v[10:13], v[160:163], v[192:195], v[10:13]
	v_mfma_f32_16x16x32_bf16 v[62:65], v[156:159], v[172:175], v[62:65]
	v_mfma_f32_16x16x32_bf16 v[58:61], v[164:167], v[172:175], v[58:61]
	v_mfma_f32_16x16x32_bf16 v[46:49], v[156:159], v[180:183], v[46:49]
	v_mfma_f32_16x16x32_bf16 v[42:45], v[164:167], v[180:183], v[42:45]
	v_mfma_f32_16x16x32_bf16 v[30:33], v[156:159], v[188:191], v[30:33]
	v_mfma_f32_16x16x32_bf16 v[26:29], v[164:167], v[188:191], v[26:29]
	v_mfma_f32_16x16x32_bf16 v[14:17], v[156:159], v[196:199], v[14:17]
	v_mfma_f32_16x16x32_bf16 v[10:13], v[164:167], v[196:199], v[10:13]
	s_setprio 0
	s_barrier
	s_add_i32 s22, s22, s43
	v_lshl_add_u64 v[144:145], v[236:237], 0, s[18:19]
	s_mov_b32 m0, s22
	s_nop 0
	global_load_lds_dwordx4 v[144:145], off
	v_lshl_add_u64 v[144:145], v[238:239], 0, s[18:19]
	s_add_i32 m0, s22, 0x2000
	s_nop 0
	global_load_lds_dwordx4 v[144:145], off
	s_waitcnt vmcnt(6)
	s_setprio 1
	s_barrier
	v_mfma_f32_16x16x32_bf16 v[54:57], v[216:219], v[168:171], v[54:57]
	v_mfma_f32_16x16x32_bf16 v[50:53], v[224:227], v[168:171], v[50:53]
	v_mfma_f32_16x16x32_bf16 v[38:41], v[216:219], v[176:179], v[38:41]
	v_mfma_f32_16x16x32_bf16 v[34:37], v[224:227], v[176:179], v[34:37]
	v_mfma_f32_16x16x32_bf16 v[22:25], v[216:219], v[184:187], v[22:25]
	v_mfma_f32_16x16x32_bf16 v[18:21], v[224:227], v[184:187], v[18:21]
	v_mfma_f32_16x16x32_bf16 v[6:9], v[216:219], v[192:195], v[6:9]
	v_mfma_f32_16x16x32_bf16 v[2:5], v[224:227], v[192:195], v[2:5]
	v_mfma_f32_16x16x32_bf16 v[54:57], v[220:223], v[172:175], v[54:57]
	s_add_u32 s12, s12, 0x100
	v_mfma_f32_16x16x32_bf16 v[50:53], v[228:231], v[172:175], v[50:53]
	s_addc_u32 s13, s13, 0
	v_mfma_f32_16x16x32_bf16 v[38:41], v[220:223], v[180:183], v[38:41]
	s_add_u32 s58, s58, 0x100
	v_mfma_f32_16x16x32_bf16 v[34:37], v[228:231], v[180:183], v[34:37]
	s_addc_u32 s59, s59, 0
	v_mfma_f32_16x16x32_bf16 v[22:25], v[220:223], v[188:191], v[22:25]
	s_cmp_ge_u32 s60, s50
	v_mfma_f32_16x16x32_bf16 v[18:21], v[228:231], v[188:191], v[18:21]
	s_mov_b32 s22, s60
	v_mfma_f32_16x16x32_bf16 v[6:9], v[220:223], v[196:199], v[6:9]
	v_mfma_f32_16x16x32_bf16 v[2:5], v[228:231], v[196:199], v[2:5]
	s_setprio 0
	s_barrier
	s_cbranch_scc0 .LBB0_2252
; __device__ __forceinline__ unsigned cvt_pk_bf16(float lo, float hi) { unsigned r; asm volatile("v_cvt_pk_bf16_f32 %0, %1, %2" : "=v"(r) : "v"(lo), "v"(hi)); return r; }
;     __device__ __forceinline__ void init(f32x4 (&acc)[2][2][4][2], const Unit& u, int wc, int fq) const {
;         const int col0 = u.pn * BM + wc * 32 + 8 * fq;
; #pragma unroll
;         for (int b = 0; b < 2; ++b)
; #pragma unroll
;             for (int n = 0; n < 2; ++n) { const f32x4 bv = *(const f32x4*)(bias + col0 + b * HALF + 4 * n);
;     __device__ __forceinline__ void operator()(const f32x4 (&acc)[2][2][4][2], const Unit& u, int wr, int wc, int fr, int fq) const {
;         const int row0 = u.pm * BM + wr * 64 + fr, col0 = u.pn * BM + wc * 32 + 8 * fq;
; #pragma unroll
;         for (int ai = 0; ai < 2; ++ai)
; #pragma unroll
;             for (int m = 0; m < 4; ++m) { bf16_t* rowp = O + (size_t)(row0 + ai * HALF + m * 16) * ldc + col0;
; #pragma unroll
;                 for (int bj = 0; bj < 2; ++bj) { const f32x4 v0 = acc[ai][bj][m][0], v1 = acc[ai][bj][m][1];
;                     u32x4 w; w[0] = cvt_pk_bf16(v0[0], v0[1]); w[1] = cvt_pk_bf16(v0[2], v0[3]); w[2] = cvt_pk_bf16(v1[0], v1[1]); w[3] = cvt_pk_bf16(v1[2], v1[3]);
;                     *(u32x4*)(rowp + bj * HALF) = w; } }
	s_nop 0
	s_nop 0
	s_nop 0
	s_nop 0
	s_nop 0
	s_nop 0
	s_nop 0
	s_nop 0
	s_nop 0
	s_nop 0
	s_nop 0
	s_nop 0
	s_nop 0
	s_nop 0
	s_nop 0
	v_lshl_add_u32 v152, s56, 8, v147
	v_lshl_or_b32 v144, s57, 8, v149
	v_ashrrev_i32_e32 v153, 31, v152
	v_ashrrev_i32_e32 v145, 31, v144
	v_lshlrev_b64 v[154:155], 11, v[152:153]
	v_lshl_add_u64 v[154:155], s[4:5], 0, v[154:155]
	v_lshlrev_b64 v[156:157], 1, v[144:145]
	v_lshl_add_u64 v[144:145], v[154:155], 0, v[156:157]
	v_cvt_pk_bf16_f32 v126, v126, v127
	v_cvt_pk_bf16_f32 v127, v128, v129
	v_cvt_pk_bf16_f32 v128, v122, v123
	v_cvt_pk_bf16_f32 v129, v124, v125
	global_store_dwordx4 v[144:145], v[126:129], off
	v_cvt_pk_bf16_f32 v118, v118, v119
	v_cvt_pk_bf16_f32 v119, v120, v121
	v_cvt_pk_bf16_f32 v120, v114, v115
	v_or_b32_e32 v114, 16, v152
	v_ashrrev_i32_e32 v115, 31, v114
	v_lshlrev_b64 v[114:115], 11, v[114:115]
	v_lshl_add_u64 v[114:115], s[4:5], 0, v[114:115]
	v_lshl_add_u64 v[114:115], v[114:115], 0, v[156:157]
	v_cvt_pk_bf16_f32 v121, v116, v117
	global_store_dwordx4 v[144:145], v[118:121], off offset:256
	v_cvt_pk_bf16_f32 v110, v110, v111
	v_cvt_pk_bf16_f32 v111, v112, v113
	v_cvt_pk_bf16_f32 v112, v106, v107
	v_cvt_pk_bf16_f32 v113, v108, v109
	global_store_dwordx4 v[114:115], v[110:113], off
	v_cvt_pk_bf16_f32 v102, v102, v103
	v_cvt_pk_bf16_f32 v103, v104, v105
	v_cvt_pk_bf16_f32 v104, v98, v99
	v_or_b32_e32 v98, 32, v152
	v_ashrrev_i32_e32 v99, 31, v98
	v_lshlrev_b64 v[98:99], 11, v[98:99]
	v_lshl_add_u64 v[98:99], s[4:5], 0, v[98:99]
	v_lshl_add_u64 v[98:99], v[98:99], 0, v[156:157]
	v_cvt_pk_bf16_f32 v105, v100, v101
	global_store_dwordx4 v[114:115], v[102:105], off offset:256
	v_cvt_pk_bf16_f32 v94, v94, v95
	v_cvt_pk_bf16_f32 v95, v96, v97
	v_cvt_pk_bf16_f32 v96, v90, v91
	v_cvt_pk_bf16_f32 v97, v92, v93
	global_store_dwordx4 v[98:99], v[94:97], off
	v_cvt_pk_bf16_f32 v86, v86, v87
	v_cvt_pk_bf16_f32 v87, v88, v89
	v_cvt_pk_bf16_f32 v88, v82, v83
	v_or_b32_e32 v82, 48, v152
	v_ashrrev_i32_e32 v83, 31, v82
	v_lshlrev_b64 v[82:83], 11, v[82:83]
	v_lshl_add_u64 v[82:83], s[4:5], 0, v[82:83]
	v_lshl_add_u64 v[82:83], v[82:83], 0, v[156:157]
	s_mov_b64 s[0:1], 0x40000
	v_cvt_pk_bf16_f32 v89, v84, v85
	global_store_dwordx4 v[98:99], v[86:89], off offset:256
	v_cvt_pk_bf16_f32 v78, v78, v79
	v_cvt_pk_bf16_f32 v79, v80, v81
	v_cvt_pk_bf16_f32 v80, v74, v75
	v_cvt_pk_bf16_f32 v81, v76, v77
	global_store_dwordx4 v[82:83], v[78:81], off
	v_cvt_pk_bf16_f32 v70, v70, v71
	v_cvt_pk_bf16_f32 v71, v72, v73
	v_cvt_pk_bf16_f32 v72, v66, v67
	v_cvt_pk_bf16_f32 v73, v68, v69
	global_store_dwordx4 v[82:83], v[70:73], off offset:256
	v_lshl_add_u64 v[66:67], v[144:145], 0, s[0:1]
	v_cvt_pk_bf16_f32 v62, v62, v63
	v_cvt_pk_bf16_f32 v63, v64, v65
	v_cvt_pk_bf16_f32 v64, v58, v59
	v_add_co_u32_e64 v58, s[0:1], s82, v144
	v_cvt_pk_bf16_f32 v65, v60, v61
	s_and_b64 vcc, exec, vcc
	s_nop 0
	v_addc_co_u32_e64 v59, s[0:1], 0, v145, s[0:1]
	s_mov_b64 s[0:1], 0x48000
	global_store_dwordx4 v[58:59], v[62:65], off
	v_cvt_pk_bf16_f32 v54, v54, v55
	v_cvt_pk_bf16_f32 v55, v56, v57
	v_cvt_pk_bf16_f32 v56, v50, v51
	v_lshl_add_u64 v[50:51], v[144:145], 0, s[0:1]
	s_mov_b32 s0, 0x48000
	v_cvt_pk_bf16_f32 v57, v52, v53
	global_store_dwordx4 v[66:67], v[54:57], off offset:256
	v_cvt_pk_bf16_f32 v46, v46, v47
	v_cvt_pk_bf16_f32 v47, v48, v49
	v_cvt_pk_bf16_f32 v48, v42, v43
	v_add_co_u32_e64 v42, s[0:1], s0, v144
	v_cvt_pk_bf16_f32 v49, v44, v45
	s_nop 1
	v_addc_co_u32_e64 v43, s[0:1], 0, v145, s[0:1]
	s_mov_b64 s[0:1], 0x50000
	global_store_dwordx4 v[42:43], v[46:49], off
	v_cvt_pk_bf16_f32 v38, v38, v39
	v_cvt_pk_bf16_f32 v39, v40, v41
	v_cvt_pk_bf16_f32 v40, v34, v35
	v_lshl_add_u64 v[34:35], v[144:145], 0, s[0:1]
	s_mov_b32 s0, 0x50000
	v_cvt_pk_bf16_f32 v41, v36, v37
	global_store_dwordx4 v[50:51], v[38:41], off offset:256
	v_cvt_pk_bf16_f32 v30, v30, v31
	v_cvt_pk_bf16_f32 v31, v32, v33
	v_cvt_pk_bf16_f32 v32, v26, v27
	v_add_co_u32_e64 v26, s[0:1], s0, v144
	v_cvt_pk_bf16_f32 v33, v28, v29
	s_nop 1
	v_addc_co_u32_e64 v27, s[0:1], 0, v145, s[0:1]
	s_mov_b64 s[0:1], 0x58000
	global_store_dwordx4 v[26:27], v[30:33], off
	v_cvt_pk_bf16_f32 v22, v22, v23
	v_cvt_pk_bf16_f32 v23, v24, v25
	v_cvt_pk_bf16_f32 v24, v18, v19
	v_lshl_add_u64 v[18:19], v[144:145], 0, s[0:1]
	s_mov_b32 s0, 0x58000
	v_cvt_pk_bf16_f32 v25, v20, v21
	global_store_dwordx4 v[34:35], v[22:25], off offset:256
	v_cvt_pk_bf16_f32 v14, v14, v15
	v_cvt_pk_bf16_f32 v15, v16, v17
	v_cvt_pk_bf16_f32 v16, v10, v11
	v_add_co_u32_e64 v10, s[0:1], s0, v144
	v_cvt_pk_bf16_f32 v17, v12, v13
	s_nop 1
	v_addc_co_u32_e64 v11, s[0:1], 0, v145, s[0:1]
	global_store_dwordx4 v[10:11], v[14:17], off
	v_cvt_pk_bf16_f32 v6, v6, v7
	v_cvt_pk_bf16_f32 v7, v8, v9
	v_cvt_pk_bf16_f32 v8, v2, v3
	v_cvt_pk_bf16_f32 v9, v4, v5
	s_mov_b64 s[0:1], -1
	global_store_dwordx4 v[18:19], v[6:9], off offset:256
	s_cbranch_vccz .LBB0_2244
	v_lshl_or_b32 v2, s54, 8, v149
	v_ashrrev_i32_e32 v3, 31, v2
	v_lshl_add_u64 v[6:7], v[2:3], 2, s[2:3]
	global_load_dwordx4 v[10:13], v[6:7], off offset:16
	global_load_dwordx4 v[14:17], v[6:7], off
	global_load_dwordx4 v[2:5], v[6:7], off offset:528
	s_nop 0
	global_load_dwordx4 v[6:9], v[6:7], off offset:512
	s_mov_b64 s[0:1], 0
	s_branch .LBB0_2244

; #define G8_STAGE(bufoff, gbase, voff) do { _Pragma("unroll") for (int _i = 0; _i < 2; ++_i) \
;         __builtin_amdgcn_global_load_lds((const unsigned*)((const char*)(gbase) + (voff)[_i]), (LAS unsigned*)(lds + (bufoff) + ldsw + _i * 8192), 16, 0, 0); } while (0)
; #define G8_LDA(dst, b, h) do { _Pragma("unroll") for (int m = 0; m < 4; ++m) _Pragma("unroll") for (int k = 0; k < 2; ++k) dst[m][k] = *(const LAS bf16x8*)(lds + G8_SA(b, h) + aoff + m * 2048 + k * 1024); } while (0)
; #define G8_LDB(dst, b, h) do { _Pragma("unroll") for (int n = 0; n < 2; ++n) _Pragma("unroll") for (int k = 0; k < 2; ++k) dst[n][k] = *(const LAS bf16x8*)(lds + G8_SB(b, h) + boff + n * 2048 + k * 1024); } while (0)
; #define G8_MMA(ai, bj, At, Bt) do { __builtin_amdgcn_s_setprio(1); _Pragma("unroll") for (int m = 0; m < 4; ++m) _Pragma("unroll") for (int n = 0; n < 2; ++n) _Pragma("unroll") for (int k = 0; k < 2; ++k) \
;         acc[ai][bj][m][n] = __builtin_amdgcn_mfma_f32_16x16x32_bf16(Bt[n][k], At[m][k], acc[ai][bj][m][n], 0, 0, 0); __builtin_amdgcn_s_setprio(0); } while (0)
; #define G8_WAIT_V(n) asm volatile("s_waitcnt vmcnt(" #n ")" ::: "memory")
; #define G8_WAIT_L(n) asm volatile("s_waitcnt lgkmcnt(" #n ")" ::: "memory")
; #define G8_BAR __builtin_amdgcn_s_barrier()
; #define G8_SCHED __builtin_amdgcn_sched_barrier(0)
; template <class Epi, class Sched>
; __device__ __forceinline__ void gemm_phase(LAS unsigned char* lds, const int K, const Sched& S, const Epi& E) {
;     ...
;             const char* a1 = cA + (size_t)(t + 1) * kstep;
;             const char* a2 = last ? nA : cA + (size_t)(t + 2) * kstep; const char* b2 = last ? nB : cB + (size_t)(t + 2) * kstep;
;             const char* a3 = a2 + kstep; const char* b3 = b2 + kstep;
;             G8_LDB(B0, 0, 0); G8_SCHED; G8_LDA(At, 0, 0); G8_STAGE(G8_SA(1, 1), a1, oc[1]);
;             if (last && has_next) S.aoff(nxt, tid, oc);
;             G8_WAIT_L(8); G8_BAR; G8_WAIT_L(0); G8_MMA(0, 0, At, B0); G8_BAR; G8_SCHED;
;             G8_LDB(B1, 0, 1); G8_STAGE(G8_SB(0, 0), b2, voffB);
;             G8_BAR; G8_WAIT_L(0); G8_MMA(0, 1, At, B1); G8_BAR;
;             G8_LDA(At, 0, 1); G8_STAGE(G8_SA(0, 0), a2, oc[0]);
;             G8_BAR; G8_WAIT_L(0); G8_MMA(1, 0, At, B0); G8_BAR; G8_SCHED;
;             G8_STAGE(G8_SB(0, 1), b2 + hstep, voffB);
;             G8_WAIT_V(6); G8_BAR; G8_MMA(1, 1, At, B1); G8_BAR;
.LBB0_2526:
	s_add_u32 s34, s22, 0x80
	s_waitcnt lgkmcnt(8)
	s_barrier
	s_waitcnt lgkmcnt(0)
	s_addc_u32 s35, s23, 0
	s_and_b64 s[24:25], s[24:25], exec
	s_cselect_b32 s35, s1, s35
	s_cselect_b32 s34, s0, s34
	s_cselect_b32 s25, s13, s56
	s_cselect_b32 s24, s12, s55
	s_setprio 1
	s_waitcnt lgkmcnt(0)
	v_mfma_f32_16x16x32_bf16 v[126:129], v[130:133], v[170:173], v[126:129]
	v_mfma_f32_16x16x32_bf16 v[122:125], v[138:141], v[170:173], v[122:125]
	v_mfma_f32_16x16x32_bf16 v[110:113], v[130:133], v[162:165], v[110:113]
	v_mfma_f32_16x16x32_bf16 v[106:109], v[138:141], v[162:165], v[106:109]
	v_mfma_f32_16x16x32_bf16 v[94:97], v[130:133], v[154:157], v[94:97]
	v_mfma_f32_16x16x32_bf16 v[90:93], v[138:141], v[154:157], v[90:93]
	v_mfma_f32_16x16x32_bf16 v[78:81], v[130:133], v[146:149], v[78:81]
	v_mfma_f32_16x16x32_bf16 v[74:77], v[138:141], v[146:149], v[74:77]
	v_mfma_f32_16x16x32_bf16 v[126:129], v[134:137], v[174:177], v[126:129]
	v_mfma_f32_16x16x32_bf16 v[122:125], v[142:145], v[174:177], v[122:125]
	v_mfma_f32_16x16x32_bf16 v[110:113], v[134:137], v[166:169], v[110:113]
	v_mfma_f32_16x16x32_bf16 v[106:109], v[142:145], v[166:169], v[106:109]
	v_mfma_f32_16x16x32_bf16 v[94:97], v[134:137], v[158:161], v[94:97]
	v_mfma_f32_16x16x32_bf16 v[90:93], v[142:145], v[158:161], v[90:93]
	v_mfma_f32_16x16x32_bf16 v[78:81], v[134:137], v[150:153], v[78:81]
	v_mfma_f32_16x16x32_bf16 v[74:77], v[142:145], v[150:153], v[74:77]
	s_setprio 0
	s_barrier
	s_add_i32 s60, 0, 0x14000
	s_mov_b32 m0, s43
	v_add_u32_e32 v183, s60, v198
	v_lshl_add_u64 v[232:233], s[24:25], 0, v[178:179]
	ds_read_b128 v[216:219], v183
	ds_read_b128 v[220:223], v183 offset:1024
	ds_read_b128 v[224:227], v183 offset:2048
	ds_read_b128 v[228:231], v183 offset:3072
	global_load_lds_dwordx4 v[232:233], off
	v_lshl_add_u64 v[234:235], s[24:25], 0, v[180:181]
	s_mov_b32 m0, s44
	s_nop 0
	global_load_lds_dwordx4 v[234:235], off
	s_setprio 1
	s_barrier
	s_waitcnt lgkmcnt(0)
	v_mfma_f32_16x16x32_bf16 v[118:121], v[216:219], v[170:173], v[118:121]
	v_mfma_f32_16x16x32_bf16 v[114:117], v[224:227], v[170:173], v[114:117]
	v_mfma_f32_16x16x32_bf16 v[102:105], v[216:219], v[162:165], v[102:105]
	v_mfma_f32_16x16x32_bf16 v[98:101], v[224:227], v[162:165], v[98:101]
	v_mfma_f32_16x16x32_bf16 v[86:89], v[216:219], v[154:157], v[86:89]
	v_mfma_f32_16x16x32_bf16 v[82:85], v[224:227], v[154:157], v[82:85]
	v_mfma_f32_16x16x32_bf16 v[70:73], v[216:219], v[146:149], v[70:73]
	v_mfma_f32_16x16x32_bf16 v[66:69], v[224:227], v[146:149], v[66:69]
	v_mfma_f32_16x16x32_bf16 v[118:121], v[220:223], v[174:177], v[118:121]
	s_mov_b32 m0, s42
	v_mfma_f32_16x16x32_bf16 v[114:117], v[228:231], v[174:177], v[114:117]
	v_mfma_f32_16x16x32_bf16 v[102:105], v[220:223], v[166:169], v[102:105]
	v_mfma_f32_16x16x32_bf16 v[98:101], v[228:231], v[166:169], v[98:101]
	v_mfma_f32_16x16x32_bf16 v[86:89], v[220:223], v[158:161], v[86:89]
	v_mfma_f32_16x16x32_bf16 v[82:85], v[228:231], v[158:161], v[82:85]
	v_mfma_f32_16x16x32_bf16 v[70:73], v[220:223], v[150:153], v[70:73]
	v_mfma_f32_16x16x32_bf16 v[66:69], v[228:231], v[150:153], v[66:69]
	s_setprio 0
	s_barrier
	ds_read_b128 v[146:149], v200 offset:16384
	ds_read_b128 v[150:153], v200 offset:17408
	ds_read_b128 v[154:157], v200 offset:18432
	ds_read_b128 v[158:161], v200 offset:19456
	ds_read_b128 v[162:165], v200 offset:20480
	ds_read_b128 v[166:169], v200 offset:21504
	ds_read_b128 v[170:173], v200 offset:22528
	ds_read_b128 v[174:177], v200 offset:23552
	global_load_lds_dwordx4 v0, s[34:35]
	s_mov_b32 m0, s45
	v_mov_b32_e32 v183, v1
	global_load_lds_dwordx4 v182, s[34:35]
	s_barrier
	s_waitcnt lgkmcnt(0)
	v_lshl_add_u64 v[236:237], s[34:35], 0, v[0:1]
	v_lshl_add_u64 v[238:239], s[34:35], 0, v[182:183]
	s_setprio 1
	s_waitcnt lgkmcnt(0)
	v_mfma_f32_16x16x32_bf16 v[62:65], v[130:133], v[146:149], v[62:65]
	v_mfma_f32_16x16x32_bf16 v[58:61], v[138:141], v[146:149], v[58:61]
	v_mfma_f32_16x16x32_bf16 v[46:49], v[130:133], v[154:157], v[46:49]
	v_mfma_f32_16x16x32_bf16 v[42:45], v[138:141], v[154:157], v[42:45]
	v_mfma_f32_16x16x32_bf16 v[30:33], v[130:133], v[162:165], v[30:33]
	v_mfma_f32_16x16x32_bf16 v[26:29], v[138:141], v[162:165], v[26:29]
	v_mfma_f32_16x16x32_bf16 v[14:17], v[130:133], v[170:173], v[14:17]
	v_mfma_f32_16x16x32_bf16 v[10:13], v[138:141], v[170:173], v[10:13]
	v_mfma_f32_16x16x32_bf16 v[62:65], v[134:137], v[150:153], v[62:65]
	v_mfma_f32_16x16x32_bf16 v[58:61], v[142:145], v[150:153], v[58:61]
	v_mfma_f32_16x16x32_bf16 v[46:49], v[134:137], v[158:161], v[46:49]
	v_mfma_f32_16x16x32_bf16 v[42:45], v[142:145], v[158:161], v[42:45]
	v_mfma_f32_16x16x32_bf16 v[30:33], v[134:137], v[166:169], v[30:33]
	v_mfma_f32_16x16x32_bf16 v[26:29], v[142:145], v[166:169], v[26:29]
	v_mfma_f32_16x16x32_bf16 v[14:17], v[134:137], v[174:177], v[14:17]
	v_mfma_f32_16x16x32_bf16 v[10:13], v[142:145], v[174:177], v[10:13]
	s_setprio 0
	s_barrier
	s_add_u32 s58, s24, 0x40000
	s_addc_u32 s59, s25, 0
	s_add_i32 s60, s60, s41
	v_lshl_add_u64 v[130:131], s[58:59], 0, v[178:179]
	s_mov_b32 m0, s60
	s_nop 0
	global_load_lds_dwordx4 v[130:131], off
	v_lshl_add_u64 v[130:131], s[58:59], 0, v[180:181]
	s_add_i32 m0, s60, 0x2000
	s_nop 0
	global_load_lds_dwordx4 v[130:131], off
	s_waitcnt vmcnt(6)
	s_setprio 1
	s_barrier
; #define G8_STAGE(bufoff, gbase, voff) do { _Pragma("unroll") for (int _i = 0; _i < 2; ++_i) \
;         __builtin_amdgcn_global_load_lds((const unsigned*)((const char*)(gbase) + (voff)[_i]), (LAS unsigned*)(lds + (bufoff) + ldsw + _i * 8192), 16, 0, 0); } while (0)
; #define G8_LDA(dst, b, h) do { _Pragma("unroll") for (int m = 0; m < 4; ++m) _Pragma("unroll") for (int k = 0; k < 2; ++k) dst[m][k] = *(const LAS bf16x8*)(lds + G8_SA(b, h) + aoff + m * 2048 + k * 1024); } while (0)
; #define G8_LDB(dst, b, h) do { _Pragma("unroll") for (int n = 0; n < 2; ++n) _Pragma("unroll") for (int k = 0; k < 2; ++k) dst[n][k] = *(const LAS bf16x8*)(lds + G8_SB(b, h) + boff + n * 2048 + k * 1024); } while (0)
; #define G8_MMA(ai, bj, At, Bt) do { __builtin_amdgcn_s_setprio(1); _Pragma("unroll") for (int m = 0; m < 4; ++m) _Pragma("unroll") for (int n = 0; n < 2; ++n) _Pragma("unroll") for (int k = 0; k < 2; ++k) \
;         acc[ai][bj][m][n] = __builtin_amdgcn_mfma_f32_16x16x32_bf16(Bt[n][k], At[m][k], acc[ai][bj][m][n], 0, 0, 0); __builtin_amdgcn_s_setprio(0); } while (0)
; #define G8_WAIT_V(n) asm volatile("s_waitcnt vmcnt(" #n ")" ::: "memory")
; #define G8_WAIT_L(n) asm volatile("s_waitcnt lgkmcnt(" #n ")" ::: "memory")
; #define G8_BAR __builtin_amdgcn_s_barrier()
; #define G8_SCHED __builtin_amdgcn_sched_barrier(0)
; template <class Epi, class Sched>
; __device__ __forceinline__ void gemm_phase(LAS unsigned char* lds, const int K, const Sched& S, const Epi& E) {
;     ...
;             G8_WAIT_V(6); G8_BAR; G8_MMA(1, 1, At, B1); G8_BAR;
;             G8_LDB(B0, 1, 0); G8_SCHED; G8_LDA(At, 1, 0); G8_STAGE(G8_SA(0, 1), a2, oc[1]);
;             G8_WAIT_L(8); G8_BAR; G8_WAIT_L(0); G8_MMA(0, 0, At, B0); G8_BAR; G8_SCHED;
;             G8_LDB(B1, 1, 1); G8_STAGE(G8_SB(1, 0), b3, voffB);
;             G8_BAR; G8_WAIT_L(0); G8_MMA(0, 1, At, B1); G8_BAR;
	v_mfma_f32_16x16x32_bf16 v[54:57], v[216:219], v[146:149], v[54:57]
	v_mfma_f32_16x16x32_bf16 v[50:53], v[224:227], v[146:149], v[50:53]
	v_mfma_f32_16x16x32_bf16 v[38:41], v[216:219], v[154:157], v[38:41]
	v_mfma_f32_16x16x32_bf16 v[34:37], v[224:227], v[154:157], v[34:37]
	v_mfma_f32_16x16x32_bf16 v[22:25], v[216:219], v[162:165], v[22:25]
	v_mfma_f32_16x16x32_bf16 v[18:21], v[224:227], v[162:165], v[18:21]
	v_mfma_f32_16x16x32_bf16 v[6:9], v[216:219], v[170:173], v[6:9]
	v_mfma_f32_16x16x32_bf16 v[2:5], v[224:227], v[170:173], v[2:5]
	v_mfma_f32_16x16x32_bf16 v[54:57], v[220:223], v[150:153], v[54:57]
	s_add_i32 s58, 0, 0x18000
	v_mfma_f32_16x16x32_bf16 v[50:53], v[228:231], v[150:153], v[50:53]
	v_add_u32_e32 v142, s58, v198
	v_mfma_f32_16x16x32_bf16 v[38:41], v[220:223], v[158:161], v[38:41]
	v_mfma_f32_16x16x32_bf16 v[34:37], v[228:231], v[158:161], v[34:37]
	v_mfma_f32_16x16x32_bf16 v[22:25], v[220:223], v[166:169], v[22:25]
	v_mfma_f32_16x16x32_bf16 v[18:21], v[228:231], v[166:169], v[18:21]
	v_mfma_f32_16x16x32_bf16 v[6:9], v[220:223], v[174:177], v[6:9]
	v_mfma_f32_16x16x32_bf16 v[2:5], v[228:231], v[174:177], v[2:5]
	s_setprio 0
	s_barrier
	ds_read_b128 v[130:133], v142
	ds_read_b128 v[134:137], v142 offset:1024
	ds_read_b128 v[138:141], v142 offset:2048
	ds_read_b128 v[142:145], v142 offset:3072
	s_mov_b32 m0, s46
	v_lshl_add_u64 v[190:191], s[34:35], 0, v[190:191]
	ds_read_b128 v[146:149], v200 offset:32768
	ds_read_b128 v[150:153], v200 offset:33792
	ds_read_b128 v[154:157], v200 offset:34816
	ds_read_b128 v[158:161], v200 offset:35840
	ds_read_b128 v[162:165], v200 offset:36864
	ds_read_b128 v[166:169], v200 offset:37888
	ds_read_b128 v[170:173], v200 offset:38912
	ds_read_b128 v[174:177], v200 offset:39936
	global_load_lds_dwordx4 v[190:191], off
	v_lshl_add_u64 v[190:191], s[34:35], 0, v[186:187]
	s_mov_b32 m0, s47
	s_nop 0
	global_load_lds_dwordx4 v[190:191], off
	s_waitcnt lgkmcnt(8)
	s_setprio 1
	s_barrier
	s_waitcnt lgkmcnt(0)
	v_mfma_f32_16x16x32_bf16 v[126:129], v[130:133], v[146:149], v[126:129]
	v_mfma_f32_16x16x32_bf16 v[122:125], v[138:141], v[146:149], v[122:125]
	v_mfma_f32_16x16x32_bf16 v[110:113], v[130:133], v[154:157], v[110:113]
	v_mfma_f32_16x16x32_bf16 v[106:109], v[138:141], v[154:157], v[106:109]
	v_mfma_f32_16x16x32_bf16 v[94:97], v[130:133], v[162:165], v[94:97]
	v_mfma_f32_16x16x32_bf16 v[90:93], v[138:141], v[162:165], v[90:93]
	v_mfma_f32_16x16x32_bf16 v[78:81], v[130:133], v[170:173], v[78:81]
	v_mfma_f32_16x16x32_bf16 v[74:77], v[138:141], v[170:173], v[74:77]
	v_mfma_f32_16x16x32_bf16 v[126:129], v[134:137], v[150:153], v[126:129]
	v_mfma_f32_16x16x32_bf16 v[122:125], v[142:145], v[150:153], v[122:125]
	v_mfma_f32_16x16x32_bf16 v[110:113], v[134:137], v[158:161], v[110:113]
	v_mfma_f32_16x16x32_bf16 v[106:109], v[142:145], v[158:161], v[106:109]
	v_mfma_f32_16x16x32_bf16 v[94:97], v[134:137], v[166:169], v[94:97]
	v_mfma_f32_16x16x32_bf16 v[90:93], v[142:145], v[166:169], v[90:93]
	v_mfma_f32_16x16x32_bf16 v[78:81], v[134:137], v[174:177], v[78:81]
	v_mfma_f32_16x16x32_bf16 v[74:77], v[142:145], v[174:177], v[74:77]
	s_setprio 0
	s_barrier
	s_add_i32 s34, 0, 0x1c000
	s_add_i32 s35, s58, s41
	v_add_u32_e32 v183, s34, v198
	v_lshl_add_u64 v[190:191], v[232:233], 0, s[18:19]
	s_mov_b32 m0, s35
	ds_read_b128 v[216:219], v183
	ds_read_b128 v[220:223], v183 offset:1024
	ds_read_b128 v[224:227], v183 offset:2048
	ds_read_b128 v[228:231], v183 offset:3072
	global_load_lds_dwordx4 v[190:191], off
	v_lshl_add_u64 v[190:191], v[234:235], 0, s[18:19]
	s_add_i32 m0, s35, 0x2000
	s_nop 0
	global_load_lds_dwordx4 v[190:191], off
	s_setprio 1
	s_barrier
	s_waitcnt lgkmcnt(0)
	v_mfma_f32_16x16x32_bf16 v[118:121], v[216:219], v[146:149], v[118:121]
	v_mfma_f32_16x16x32_bf16 v[114:117], v[224:227], v[146:149], v[114:117]
	v_mfma_f32_16x16x32_bf16 v[102:105], v[216:219], v[154:157], v[102:105]
	v_mfma_f32_16x16x32_bf16 v[98:101], v[224:227], v[154:157], v[98:101]
	v_mfma_f32_16x16x32_bf16 v[86:89], v[216:219], v[162:165], v[86:89]
	v_mfma_f32_16x16x32_bf16 v[82:85], v[224:227], v[162:165], v[82:85]
	v_mfma_f32_16x16x32_bf16 v[70:73], v[216:219], v[170:173], v[70:73]
	v_mfma_f32_16x16x32_bf16 v[66:69], v[224:227], v[170:173], v[66:69]
	v_mfma_f32_16x16x32_bf16 v[118:121], v[220:223], v[150:153], v[118:121]
	s_mov_b32 m0, s49
	v_mfma_f32_16x16x32_bf16 v[114:117], v[228:231], v[150:153], v[114:117]
	v_lshl_add_u64 v[190:191], v[236:237], 0, s[18:19]
	v_mfma_f32_16x16x32_bf16 v[102:105], v[220:223], v[158:161], v[102:105]
	v_mfma_f32_16x16x32_bf16 v[98:101], v[228:231], v[158:161], v[98:101]
	v_mfma_f32_16x16x32_bf16 v[86:89], v[220:223], v[166:169], v[86:89]
	v_mfma_f32_16x16x32_bf16 v[82:85], v[228:231], v[166:169], v[82:85]
	v_mfma_f32_16x16x32_bf16 v[70:73], v[220:223], v[174:177], v[70:73]
	v_mfma_f32_16x16x32_bf16 v[66:69], v[228:231], v[174:177], v[66:69]
	s_setprio 0
	s_barrier
; #define G8_STAGE(bufoff, gbase, voff) do { _Pragma("unroll") for (int _i = 0; _i < 2; ++_i) \
;         __builtin_amdgcn_global_load_lds((const unsigned*)((const char*)(gbase) + (voff)[_i]), (LAS unsigned*)(lds + (bufoff) + ldsw + _i * 8192), 16, 0, 0); } while (0)
; #define G8_LDA(dst, b, h) do { _Pragma("unroll") for (int m = 0; m < 4; ++m) _Pragma("unroll") for (int k = 0; k < 2; ++k) dst[m][k] = *(const LAS bf16x8*)(lds + G8_SA(b, h) + aoff + m * 2048 + k * 1024); } while (0)
; #define G8_LDB(dst, b, h) do { _Pragma("unroll") for (int n = 0; n < 2; ++n) _Pragma("unroll") for (int k = 0; k < 2; ++k) dst[n][k] = *(const LAS bf16x8*)(lds + G8_SB(b, h) + boff + n * 2048 + k * 1024); } while (0)
; #define G8_WAIT_V(n) asm volatile("s_waitcnt vmcnt(" #n ")" ::: "memory")
; #define G8_WAIT_L(n) asm volatile("s_waitcnt lgkmcnt(" #n ")" ::: "memory")
; #define G8_BAR __builtin_amdgcn_s_barrier()
; #define G8_SCHED __builtin_amdgcn_sched_barrier(0)
; template <class Epi, class Sched>
; __device__ __forceinline__ void gemm_phase(LAS unsigned char* lds, const int K, const Sched& S, const Epi& E) {
;     ...
;             G8_LDB(B0, 0, 0); G8_SCHED; G8_LDA(At, 0, 0); G8_STAGE(G8_SA(1, 1), a1, oc[1]);
;             if (last && has_next) S.aoff(nxt, tid, oc);
;             G8_WAIT_L(8); G8_BAR; G8_WAIT_L(0); G8_MMA(0, 0, At, B0); G8_BAR; G8_SCHED;
;             G8_LDB(B1, 0, 1); G8_STAGE(G8_SB(0, 0), b2, voffB);
;             G8_BAR; G8_WAIT_L(0); G8_MMA(0, 1, At, B1); G8_BAR;
;             G8_LDA(At, 0, 1); G8_STAGE(G8_SA(0, 0), a2, oc[0]);
;             G8_BAR; G8_WAIT_L(0); G8_MMA(1, 0, At, B0); G8_BAR; G8_SCHED;
;             G8_STAGE(G8_SB(0, 1), b2 + hstep, voffB);
;             G8_WAIT_V(6); G8_BAR; G8_MMA(1, 1, At, B1); G8_BAR;
;             G8_LDB(B0, 1, 0); G8_SCHED; G8_LDA(At, 1, 0); G8_STAGE(G8_SA(0, 1), a2, oc[1]);
;             G8_WAIT_L(8); G8_BAR; G8_WAIT_L(0); G8_MMA(0, 0, At, B0); G8_BAR; G8_SCHED;
;             G8_LDB(B1, 1, 1); G8_STAGE(G8_SB(1, 0), b3, voffB);
;             G8_BAR; G8_WAIT_L(0); G8_MMA(0, 1, At, B1); G8_BAR;
;             G8_LDA(At, 1, 1); G8_STAGE(G8_SA(1, 0), a3, oc[0]);
;             G8_BAR; G8_WAIT_L(0); G8_MMA(1, 0, At, B0); G8_BAR; G8_SCHED;
;             G8_STAGE(G8_SB(1, 1), b3 + hstep, voffB);
;             G8_WAIT_V(6); G8_BAR; G8_MMA(1, 1, At, B1); G8_BAR;
	ds_read_b128 v[146:149], v200 offset:49152
	ds_read_b128 v[150:153], v200 offset:50176
	ds_read_b128 v[154:157], v200 offset:51200
	ds_read_b128 v[158:161], v200 offset:52224
	ds_read_b128 v[162:165], v200 offset:53248
	ds_read_b128 v[166:169], v200 offset:54272
	ds_read_b128 v[170:173], v200 offset:55296
	ds_read_b128 v[174:177], v200 offset:56320
	global_load_lds_dwordx4 v[190:191], off
	v_lshl_add_u64 v[190:191], v[238:239], 0, s[18:19]
	s_mov_b32 m0, s50
	s_nop 0
	global_load_lds_dwordx4 v[190:191], off
	s_setprio 1
	s_barrier
	s_waitcnt lgkmcnt(0)
	v_mfma_f32_16x16x32_bf16 v[62:65], v[130:133], v[146:149], v[62:65]
	v_mfma_f32_16x16x32_bf16 v[58:61], v[138:141], v[146:149], v[58:61]
	v_mfma_f32_16x16x32_bf16 v[46:49], v[130:133], v[154:157], v[46:49]
	v_mfma_f32_16x16x32_bf16 v[42:45], v[138:141], v[154:157], v[42:45]
	v_mfma_f32_16x16x32_bf16 v[30:33], v[130:133], v[162:165], v[30:33]
	v_mfma_f32_16x16x32_bf16 v[26:29], v[138:141], v[162:165], v[26:29]
	v_mfma_f32_16x16x32_bf16 v[14:17], v[130:133], v[170:173], v[14:17]
	v_mfma_f32_16x16x32_bf16 v[10:13], v[138:141], v[170:173], v[10:13]
	v_mfma_f32_16x16x32_bf16 v[62:65], v[134:137], v[150:153], v[62:65]
	v_mfma_f32_16x16x32_bf16 v[58:61], v[142:145], v[150:153], v[58:61]
	v_mfma_f32_16x16x32_bf16 v[46:49], v[134:137], v[158:161], v[46:49]
	v_mfma_f32_16x16x32_bf16 v[42:45], v[142:145], v[158:161], v[42:45]
	v_mfma_f32_16x16x32_bf16 v[30:33], v[134:137], v[166:169], v[30:33]
	v_mfma_f32_16x16x32_bf16 v[26:29], v[142:145], v[166:169], v[26:29]
	v_mfma_f32_16x16x32_bf16 v[14:17], v[134:137], v[174:177], v[14:17]
	v_mfma_f32_16x16x32_bf16 v[10:13], v[142:145], v[174:177], v[10:13]
	s_setprio 0
	s_barrier
	s_add_u32 s24, s24, 0x40080
	s_addc_u32 s25, s25, 0
	s_add_i32 s34, s34, s41
	v_lshl_add_u64 v[130:131], s[24:25], 0, v[178:179]
	s_mov_b32 m0, s34
	s_nop 0
	global_load_lds_dwordx4 v[130:131], off
	v_lshl_add_u64 v[130:131], s[24:25], 0, v[180:181]
	s_add_i32 m0, s34, 0x2000
	s_nop 0
	global_load_lds_dwordx4 v[130:131], off
	s_waitcnt vmcnt(6)
	s_setprio 1
	s_barrier
	v_mfma_f32_16x16x32_bf16 v[54:57], v[216:219], v[146:149], v[54:57]
	v_mfma_f32_16x16x32_bf16 v[50:53], v[224:227], v[146:149], v[50:53]
	v_mfma_f32_16x16x32_bf16 v[38:41], v[216:219], v[154:157], v[38:41]
	v_mfma_f32_16x16x32_bf16 v[34:37], v[224:227], v[154:157], v[34:37]
	v_mfma_f32_16x16x32_bf16 v[22:25], v[216:219], v[162:165], v[22:25]
	v_mfma_f32_16x16x32_bf16 v[18:21], v[224:227], v[162:165], v[18:21]
	v_mfma_f32_16x16x32_bf16 v[6:9], v[216:219], v[170:173], v[6:9]
	v_mfma_f32_16x16x32_bf16 v[2:5], v[224:227], v[170:173], v[2:5]
	v_mfma_f32_16x16x32_bf16 v[54:57], v[220:223], v[150:153], v[54:57]
	s_add_i32 s57, s57, 2
	v_mfma_f32_16x16x32_bf16 v[50:53], v[228:231], v[150:153], v[50:53]
	s_add_u32 s22, s22, 0x100
	v_mfma_f32_16x16x32_bf16 v[38:41], v[220:223], v[158:161], v[38:41]
	s_addc_u32 s23, s23, 0
	v_mfma_f32_16x16x32_bf16 v[34:37], v[228:231], v[158:161], v[34:37]
	s_add_u32 s55, s55, 0x100
	v_mfma_f32_16x16x32_bf16 v[22:25], v[220:223], v[166:169], v[22:25]
	s_addc_u32 s56, s56, 0
	v_mfma_f32_16x16x32_bf16 v[18:21], v[228:231], v[166:169], v[18:21]
	s_cmp_gt_u32 s57, 13
	v_mfma_f32_16x16x32_bf16 v[6:9], v[220:223], v[174:177], v[6:9]
	v_mfma_f32_16x16x32_bf16 v[2:5], v[228:231], v[174:177], v[2:5]
	s_setprio 0
	s_barrier
	s_cbranch_scc1 .LBB0_2529
.LBB0_2527:
	v_add_u32_e32 v130, 0, v198
	v_add_u32_e32 v142, 0x10000, v130
	ds_read_b128 v[130:133], v142
	ds_read_b128 v[134:137], v142 offset:1024
	ds_read_b128 v[138:141], v142 offset:2048
	ds_read_b128 v[142:145], v142 offset:3072
	s_cmp_eq_u32 s57, 12
	s_cselect_b64 s[24:25], -1, 0
	s_add_i32 m0, s42, 0xc000
	ds_read_b128 v[170:173], v200
	ds_read_b128 v[174:177], v200 offset:1024
	ds_read_b128 v[162:165], v200 offset:2048
	ds_read_b128 v[166:169], v200 offset:3072
	ds_read_b128 v[154:157], v200 offset:4096
	ds_read_b128 v[158:161], v200 offset:5120
	ds_read_b128 v[146:149], v200 offset:6144
	ds_read_b128 v[150:153], v200 offset:7168
	global_load_lds_dwordx4 v184, s[22:23]
	s_add_i32 m0, s42, 0xe000
	s_and_b64 s[34:35], s[10:11], s[24:25]
	global_load_lds_dwordx4 v186, s[22:23]
	s_andn2_b64 vcc, exec, s[34:35]
	s_cbranch_vccz .LBB0_2525
	v_mov_b32_e32 v185, v1
	v_mov_b32_e32 v187, v1
	v_mov_b64_e32 v[190:191], v[184:185]
	s_branch .LBB0_2526
	s_nop 0
	s_nop 0
	s_nop 0
	s_nop 0
	s_nop 0
	s_nop 0
	s_nop 0
	s_nop 0
	s_nop 0
	s_nop 0

; #define G8_STAGE(bufoff, gbase, voff) do { _Pragma("unroll") for (int _i = 0; _i < 2; ++_i) \
;         __builtin_amdgcn_global_load_lds((const unsigned*)((const char*)(gbase) + (voff)[_i]), (LAS unsigned*)(lds + (bufoff) + ldsw + _i * 8192), 16, 0, 0); } while (0)
; #define G8_LDA(dst, b, h) do { _Pragma("unroll") for (int m = 0; m < 4; ++m) _Pragma("unroll") for (int k = 0; k < 2; ++k) dst[m][k] = *(const LAS bf16x8*)(lds + G8_SA(b, h) + aoff + m * 2048 + k * 1024); } while (0)
; #define G8_LDB(dst, b, h) do { _Pragma("unroll") for (int n = 0; n < 2; ++n) _Pragma("unroll") for (int k = 0; k < 2; ++k) dst[n][k] = *(const LAS bf16x8*)(lds + G8_SB(b, h) + boff + n * 2048 + k * 1024); } while (0)
; #define G8_MMA(ai, bj, At, Bt) do { __builtin_amdgcn_s_setprio(1); _Pragma("unroll") for (int m = 0; m < 4; ++m) _Pragma("unroll") for (int n = 0; n < 2; ++n) _Pragma("unroll") for (int k = 0; k < 2; ++k) \
;         acc[ai][bj][m][n] = __builtin_amdgcn_mfma_f32_16x16x32_bf16(Bt[n][k], At[m][k], acc[ai][bj][m][n], 0, 0, 0); __builtin_amdgcn_s_setprio(0); } while (0)
; #define G8_WAIT_V(n) asm volatile("s_waitcnt vmcnt(" #n ")" ::: "memory")
; #define G8_WAIT_L(n) asm volatile("s_waitcnt lgkmcnt(" #n ")" ::: "memory")
; #define G8_BAR __builtin_amdgcn_s_barrier()
; #define G8_SCHED __builtin_amdgcn_sched_barrier(0)
; template <class Epi, class Sched>
; __device__ __forceinline__ void gemm_phase(LAS unsigned char* lds, const int K, const Sched& S, const Epi& E) {
;     ...
;             const char* a1 = cA + (size_t)(t + 1) * kstep;
;             const char* a2 = last ? nA : cA + (size_t)(t + 2) * kstep; const char* b2 = last ? nB : cB + (size_t)(t + 2) * kstep;
;             const char* a3 = a2 + kstep; const char* b3 = b2 + kstep;
;             G8_LDB(B0, 0, 0); G8_SCHED; G8_LDA(At, 0, 0); G8_STAGE(G8_SA(1, 1), a1, oc[1]);
;             if (last && has_next) S.aoff(nxt, tid, oc);
;             G8_WAIT_L(8); G8_BAR; G8_WAIT_L(0); G8_MMA(0, 0, At, B0); G8_BAR; G8_SCHED;
;             G8_LDB(B1, 0, 1); G8_STAGE(G8_SB(0, 0), b2, voffB);
;             G8_BAR; G8_WAIT_L(0); G8_MMA(0, 1, At, B1); G8_BAR;
;             G8_LDA(At, 0, 1); G8_STAGE(G8_SA(0, 0), a2, oc[0]);
;             G8_BAR; G8_WAIT_L(0); G8_MMA(1, 0, At, B0); G8_BAR; G8_SCHED;
;             G8_STAGE(G8_SB(0, 1), b2 + hstep, voffB);
;             G8_WAIT_V(6); G8_BAR; G8_MMA(1, 1, At, B1); G8_BAR;
.LBB0_2616:
	s_xor_b64 s[40:41], s[42:43], -1
	s_add_u32 s44, s44, 0x100
	s_addc_u32 s45, s45, 0
	s_and_b64 s[42:43], s[36:37], exec
	s_cselect_b32 s43, s1, s45
	s_cselect_b32 s42, s0, s44
	s_add_u32 s38, s22, s38
	s_addc_u32 s39, s23, s39
	s_add_u32 s38, s38, 0x100
	s_addc_u32 s39, s39, 0
	s_waitcnt lgkmcnt(8)
	s_barrier
	s_waitcnt lgkmcnt(0)
	s_and_b64 s[36:37], s[36:37], exec
	s_cselect_b32 s37, s35, s39
	s_cselect_b32 s36, s34, s38
	s_setprio 1
	s_waitcnt lgkmcnt(0)
	v_mfma_f32_16x16x32_bf16 v[126:129], v[130:133], v[170:173], v[126:129]
	v_mfma_f32_16x16x32_bf16 v[122:125], v[138:141], v[170:173], v[122:125]
	v_mfma_f32_16x16x32_bf16 v[110:113], v[130:133], v[162:165], v[110:113]
	v_mfma_f32_16x16x32_bf16 v[106:109], v[138:141], v[162:165], v[106:109]
	v_mfma_f32_16x16x32_bf16 v[94:97], v[130:133], v[154:157], v[94:97]
	v_mfma_f32_16x16x32_bf16 v[90:93], v[138:141], v[154:157], v[90:93]
	v_mfma_f32_16x16x32_bf16 v[78:81], v[130:133], v[146:149], v[78:81]
	v_mfma_f32_16x16x32_bf16 v[74:77], v[138:141], v[146:149], v[74:77]
	v_mfma_f32_16x16x32_bf16 v[126:129], v[134:137], v[174:177], v[126:129]
	v_mfma_f32_16x16x32_bf16 v[122:125], v[142:145], v[174:177], v[122:125]
	v_mfma_f32_16x16x32_bf16 v[110:113], v[134:137], v[166:169], v[110:113]
	v_mfma_f32_16x16x32_bf16 v[106:109], v[142:145], v[166:169], v[106:109]
	v_mfma_f32_16x16x32_bf16 v[94:97], v[134:137], v[158:161], v[94:97]
	v_mfma_f32_16x16x32_bf16 v[90:93], v[142:145], v[158:161], v[90:93]
	v_mfma_f32_16x16x32_bf16 v[78:81], v[134:137], v[150:153], v[78:81]
	v_mfma_f32_16x16x32_bf16 v[74:77], v[142:145], v[150:153], v[74:77]
	s_setprio 0
	s_barrier
	s_add_i32 s44, 0, 0x14000
	s_mov_b32 m0, s52
	v_add_u32_e32 v183, s44, v200
	v_lshl_add_u64 v[236:237], s[36:37], 0, v[178:179]
	ds_read_b128 v[220:223], v183
	ds_read_b128 v[224:227], v183 offset:1024
	ds_read_b128 v[228:231], v183 offset:2048
	ds_read_b128 v[232:235], v183 offset:3072
	global_load_lds_dwordx4 v[236:237], off
	v_lshl_add_u64 v[238:239], s[36:37], 0, v[180:181]
	s_mov_b32 m0, s53
	s_nop 0
	global_load_lds_dwordx4 v[238:239], off
	s_setprio 1
	s_barrier
	s_waitcnt lgkmcnt(0)
	v_mfma_f32_16x16x32_bf16 v[118:121], v[220:223], v[170:173], v[118:121]
	v_mfma_f32_16x16x32_bf16 v[114:117], v[228:231], v[170:173], v[114:117]
	v_mfma_f32_16x16x32_bf16 v[102:105], v[220:223], v[162:165], v[102:105]
	v_mfma_f32_16x16x32_bf16 v[98:101], v[228:231], v[162:165], v[98:101]
	v_mfma_f32_16x16x32_bf16 v[86:89], v[220:223], v[154:157], v[86:89]
	v_mfma_f32_16x16x32_bf16 v[82:85], v[228:231], v[154:157], v[82:85]
	v_mfma_f32_16x16x32_bf16 v[70:73], v[220:223], v[146:149], v[70:73]
	v_mfma_f32_16x16x32_bf16 v[66:69], v[228:231], v[146:149], v[66:69]
	v_mfma_f32_16x16x32_bf16 v[118:121], v[224:227], v[174:177], v[118:121]
	s_mov_b32 m0, s51
	v_mfma_f32_16x16x32_bf16 v[114:117], v[232:235], v[174:177], v[114:117]
	v_mfma_f32_16x16x32_bf16 v[102:105], v[224:227], v[166:169], v[102:105]
	v_mfma_f32_16x16x32_bf16 v[98:101], v[232:235], v[166:169], v[98:101]
	v_mfma_f32_16x16x32_bf16 v[86:89], v[224:227], v[158:161], v[86:89]
	v_mfma_f32_16x16x32_bf16 v[82:85], v[232:235], v[158:161], v[82:85]
	v_mfma_f32_16x16x32_bf16 v[70:73], v[224:227], v[150:153], v[70:73]
	v_mfma_f32_16x16x32_bf16 v[66:69], v[232:235], v[150:153], v[66:69]
	s_setprio 0
	s_barrier
	ds_read_b128 v[146:149], v216 offset:16384
	ds_read_b128 v[150:153], v216 offset:17408
	ds_read_b128 v[154:157], v216 offset:18432
	ds_read_b128 v[158:161], v216 offset:19456
	ds_read_b128 v[162:165], v216 offset:20480
	ds_read_b128 v[166:169], v216 offset:21504
	ds_read_b128 v[170:173], v216 offset:22528
	ds_read_b128 v[174:177], v216 offset:23552
	global_load_lds_dwordx4 v182, s[42:43]
	s_mov_b32 m0, s54
	v_mov_b32_e32 v183, v1
	global_load_lds_dwordx4 v184, s[42:43]
	s_barrier
	s_waitcnt lgkmcnt(0)
	v_mov_b32_e32 v185, v1
	v_lshl_add_u64 v[240:241], s[42:43], 0, v[182:183]
	v_lshl_add_u64 v[242:243], s[42:43], 0, v[184:185]
	s_setprio 1
	s_waitcnt lgkmcnt(0)
	v_mfma_f32_16x16x32_bf16 v[62:65], v[130:133], v[146:149], v[62:65]
	v_mfma_f32_16x16x32_bf16 v[58:61], v[138:141], v[146:149], v[58:61]
	v_mfma_f32_16x16x32_bf16 v[46:49], v[130:133], v[154:157], v[46:49]
	v_mfma_f32_16x16x32_bf16 v[42:45], v[138:141], v[154:157], v[42:45]
	v_mfma_f32_16x16x32_bf16 v[30:33], v[130:133], v[162:165], v[30:33]
	v_mfma_f32_16x16x32_bf16 v[26:29], v[138:141], v[162:165], v[26:29]
	v_mfma_f32_16x16x32_bf16 v[14:17], v[130:133], v[170:173], v[14:17]
	v_mfma_f32_16x16x32_bf16 v[10:13], v[138:141], v[170:173], v[10:13]
	v_mfma_f32_16x16x32_bf16 v[62:65], v[134:137], v[150:153], v[62:65]
	v_mfma_f32_16x16x32_bf16 v[58:61], v[142:145], v[150:153], v[58:61]
	v_mfma_f32_16x16x32_bf16 v[46:49], v[134:137], v[158:161], v[46:49]
	v_mfma_f32_16x16x32_bf16 v[42:45], v[142:145], v[158:161], v[42:45]
	v_mfma_f32_16x16x32_bf16 v[30:33], v[134:137], v[166:169], v[30:33]
	v_mfma_f32_16x16x32_bf16 v[26:29], v[142:145], v[166:169], v[26:29]
	v_mfma_f32_16x16x32_bf16 v[14:17], v[134:137], v[174:177], v[14:17]
	v_mfma_f32_16x16x32_bf16 v[10:13], v[142:145], v[174:177], v[10:13]
	s_setprio 0
	s_barrier
	s_add_u32 s38, s36, 0x10000
	s_addc_u32 s39, s37, 0
	s_add_i32 s44, s44, s50
	v_lshl_add_u64 v[130:131], s[38:39], 0, v[178:179]
	s_mov_b32 m0, s44
	s_nop 0
	global_load_lds_dwordx4 v[130:131], off
	v_lshl_add_u64 v[130:131], s[38:39], 0, v[180:181]
	s_add_i32 m0, s44, 0x2000
	s_nop 0
	global_load_lds_dwordx4 v[130:131], off
	s_waitcnt vmcnt(6)
	s_setprio 1
	s_barrier
; #define G8_STAGE(bufoff, gbase, voff) do { _Pragma("unroll") for (int _i = 0; _i < 2; ++_i) \
;         __builtin_amdgcn_global_load_lds((const unsigned*)((const char*)(gbase) + (voff)[_i]), (LAS unsigned*)(lds + (bufoff) + ldsw + _i * 8192), 16, 0, 0); } while (0)
; #define G8_LDA(dst, b, h) do { _Pragma("unroll") for (int m = 0; m < 4; ++m) _Pragma("unroll") for (int k = 0; k < 2; ++k) dst[m][k] = *(const LAS bf16x8*)(lds + G8_SA(b, h) + aoff + m * 2048 + k * 1024); } while (0)
; #define G8_LDB(dst, b, h) do { _Pragma("unroll") for (int n = 0; n < 2; ++n) _Pragma("unroll") for (int k = 0; k < 2; ++k) dst[n][k] = *(const LAS bf16x8*)(lds + G8_SB(b, h) + boff + n * 2048 + k * 1024); } while (0)
; #define G8_MMA(ai, bj, At, Bt) do { __builtin_amdgcn_s_setprio(1); _Pragma("unroll") for (int m = 0; m < 4; ++m) _Pragma("unroll") for (int n = 0; n < 2; ++n) _Pragma("unroll") for (int k = 0; k < 2; ++k) \
;         acc[ai][bj][m][n] = __builtin_amdgcn_mfma_f32_16x16x32_bf16(Bt[n][k], At[m][k], acc[ai][bj][m][n], 0, 0, 0); __builtin_amdgcn_s_setprio(0); } while (0)
; #define G8_WAIT_V(n) asm volatile("s_waitcnt vmcnt(" #n ")" ::: "memory")
; #define G8_WAIT_L(n) asm volatile("s_waitcnt lgkmcnt(" #n ")" ::: "memory")
; #define G8_BAR __builtin_amdgcn_s_barrier()
; #define G8_SCHED __builtin_amdgcn_sched_barrier(0)
; template <class Epi, class Sched>
; __device__ __forceinline__ void gemm_phase(LAS unsigned char* lds, const int K, const Sched& S, const Epi& E) {
;     ...
;             G8_WAIT_V(6); G8_BAR; G8_MMA(1, 1, At, B1); G8_BAR;
;             G8_LDB(B0, 1, 0); G8_SCHED; G8_LDA(At, 1, 0); G8_STAGE(G8_SA(0, 1), a2, oc[1]);
;             G8_WAIT_L(8); G8_BAR; G8_WAIT_L(0); G8_MMA(0, 0, At, B0); G8_BAR; G8_SCHED;
;             G8_LDB(B1, 1, 1); G8_STAGE(G8_SB(1, 0), b3, voffB);
;             G8_BAR; G8_WAIT_L(0); G8_MMA(0, 1, At, B1); G8_BAR;
	v_mfma_f32_16x16x32_bf16 v[54:57], v[220:223], v[146:149], v[54:57]
	v_mfma_f32_16x16x32_bf16 v[50:53], v[228:231], v[146:149], v[50:53]
	v_mfma_f32_16x16x32_bf16 v[38:41], v[220:223], v[154:157], v[38:41]
	v_mfma_f32_16x16x32_bf16 v[34:37], v[228:231], v[154:157], v[34:37]
	v_mfma_f32_16x16x32_bf16 v[22:25], v[220:223], v[162:165], v[22:25]
	v_mfma_f32_16x16x32_bf16 v[18:21], v[228:231], v[162:165], v[18:21]
	v_mfma_f32_16x16x32_bf16 v[6:9], v[220:223], v[170:173], v[6:9]
	v_mfma_f32_16x16x32_bf16 v[2:5], v[228:231], v[170:173], v[2:5]
	v_mfma_f32_16x16x32_bf16 v[54:57], v[224:227], v[150:153], v[54:57]
	s_add_i32 s38, 0, 0x18000
	v_mfma_f32_16x16x32_bf16 v[50:53], v[232:235], v[150:153], v[50:53]
	v_add_u32_e32 v142, s38, v200
	v_mfma_f32_16x16x32_bf16 v[38:41], v[224:227], v[158:161], v[38:41]
	v_mfma_f32_16x16x32_bf16 v[34:37], v[232:235], v[158:161], v[34:37]
	v_mfma_f32_16x16x32_bf16 v[22:25], v[224:227], v[166:169], v[22:25]
	v_mfma_f32_16x16x32_bf16 v[18:21], v[232:235], v[166:169], v[18:21]
	v_mfma_f32_16x16x32_bf16 v[6:9], v[224:227], v[174:177], v[6:9]
	v_mfma_f32_16x16x32_bf16 v[2:5], v[232:235], v[174:177], v[2:5]
	s_setprio 0
	s_barrier
	ds_read_b128 v[130:133], v142
	ds_read_b128 v[134:137], v142 offset:1024
	ds_read_b128 v[138:141], v142 offset:2048
	ds_read_b128 v[142:145], v142 offset:3072
	s_mov_b32 m0, s55
	v_lshl_add_u64 v[220:221], s[42:43], 0, v[0:1]
	ds_read_b128 v[146:149], v216 offset:32768
	ds_read_b128 v[150:153], v216 offset:33792
	ds_read_b128 v[154:157], v216 offset:34816
	ds_read_b128 v[158:161], v216 offset:35840
	ds_read_b128 v[162:165], v216 offset:36864
	ds_read_b128 v[166:169], v216 offset:37888
	ds_read_b128 v[170:173], v216 offset:38912
	ds_read_b128 v[174:177], v216 offset:39936
	global_load_lds_dwordx4 v[220:221], off
	v_lshl_add_u64 v[220:221], s[42:43], 0, v[186:187]
	s_mov_b32 m0, s56
	s_nop 0
	global_load_lds_dwordx4 v[220:221], off
	s_waitcnt lgkmcnt(8)
	s_setprio 1
	s_barrier
	s_waitcnt lgkmcnt(0)
	v_mfma_f32_16x16x32_bf16 v[126:129], v[130:133], v[146:149], v[126:129]
	v_mfma_f32_16x16x32_bf16 v[122:125], v[138:141], v[146:149], v[122:125]
	v_mfma_f32_16x16x32_bf16 v[110:113], v[130:133], v[154:157], v[110:113]
	v_mfma_f32_16x16x32_bf16 v[106:109], v[138:141], v[154:157], v[106:109]
	v_mfma_f32_16x16x32_bf16 v[94:97], v[130:133], v[162:165], v[94:97]
	v_mfma_f32_16x16x32_bf16 v[90:93], v[138:141], v[162:165], v[90:93]
	v_mfma_f32_16x16x32_bf16 v[78:81], v[130:133], v[170:173], v[78:81]
	v_mfma_f32_16x16x32_bf16 v[74:77], v[138:141], v[170:173], v[74:77]
	v_mfma_f32_16x16x32_bf16 v[126:129], v[134:137], v[150:153], v[126:129]
	v_mfma_f32_16x16x32_bf16 v[122:125], v[142:145], v[150:153], v[122:125]
	v_mfma_f32_16x16x32_bf16 v[110:113], v[134:137], v[158:161], v[110:113]
	v_mfma_f32_16x16x32_bf16 v[106:109], v[142:145], v[158:161], v[106:109]
	v_mfma_f32_16x16x32_bf16 v[94:97], v[134:137], v[166:169], v[94:97]
	v_mfma_f32_16x16x32_bf16 v[90:93], v[142:145], v[166:169], v[90:93]
	v_mfma_f32_16x16x32_bf16 v[78:81], v[134:137], v[174:177], v[78:81]
	v_mfma_f32_16x16x32_bf16 v[74:77], v[142:145], v[174:177], v[74:77]
	s_setprio 0
	s_barrier
	s_add_i32 s39, 0, 0x1c000
	s_add_i32 s38, s38, s50
	v_add_u32_e32 v183, s39, v200
	v_lshl_add_u64 v[236:237], v[236:237], 0, s[18:19]
	s_mov_b32 m0, s38
	ds_read_b128 v[220:223], v183
	ds_read_b128 v[224:227], v183 offset:1024
	ds_read_b128 v[228:231], v183 offset:2048
	ds_read_b128 v[232:235], v183 offset:3072
	global_load_lds_dwordx4 v[236:237], off
	v_lshl_add_u64 v[236:237], v[238:239], 0, s[18:19]
	s_add_i32 m0, s38, 0x2000
	s_nop 0
	global_load_lds_dwordx4 v[236:237], off
	s_setprio 1
	s_barrier
; #define G8_STAGE(bufoff, gbase, voff) do { _Pragma("unroll") for (int _i = 0; _i < 2; ++_i) \
;         __builtin_amdgcn_global_load_lds((const unsigned*)((const char*)(gbase) + (voff)[_i]), (LAS unsigned*)(lds + (bufoff) + ldsw + _i * 8192), 16, 0, 0); } while (0)
; #define G8_LDA(dst, b, h) do { _Pragma("unroll") for (int m = 0; m < 4; ++m) _Pragma("unroll") for (int k = 0; k < 2; ++k) dst[m][k] = *(const LAS bf16x8*)(lds + G8_SA(b, h) + aoff + m * 2048 + k * 1024); } while (0)
; #define G8_MMA(ai, bj, At, Bt) do { __builtin_amdgcn_s_setprio(1); _Pragma("unroll") for (int m = 0; m < 4; ++m) _Pragma("unroll") for (int n = 0; n < 2; ++n) _Pragma("unroll") for (int k = 0; k < 2; ++k) \
;         acc[ai][bj][m][n] = __builtin_amdgcn_mfma_f32_16x16x32_bf16(Bt[n][k], At[m][k], acc[ai][bj][m][n], 0, 0, 0); __builtin_amdgcn_s_setprio(0); } while (0)
; #define G8_WAIT_V(n) asm volatile("s_waitcnt vmcnt(" #n ")" ::: "memory")
; #define G8_WAIT_L(n) asm volatile("s_waitcnt lgkmcnt(" #n ")" ::: "memory")
; #define G8_BAR __builtin_amdgcn_s_barrier()
; #define G8_SCHED __builtin_amdgcn_sched_barrier(0)
; template <class Epi, class Sched>
; __device__ __forceinline__ void gemm_phase(LAS unsigned char* lds, const int K, const Sched& S, const Epi& E) {
;     ...
;             G8_BAR; G8_WAIT_L(0); G8_MMA(0, 1, At, B1); G8_BAR;
;             G8_LDA(At, 1, 1); G8_STAGE(G8_SA(1, 0), a3, oc[0]);
;             G8_BAR; G8_WAIT_L(0); G8_MMA(1, 0, At, B0); G8_BAR; G8_SCHED;
;             G8_STAGE(G8_SB(1, 1), b3 + hstep, voffB);
;             G8_WAIT_V(6); G8_BAR; G8_MMA(1, 1, At, B1); G8_BAR;
;         }
	s_waitcnt lgkmcnt(0)
	v_mfma_f32_16x16x32_bf16 v[118:121], v[220:223], v[146:149], v[118:121]
	v_mfma_f32_16x16x32_bf16 v[114:117], v[228:231], v[146:149], v[114:117]
	v_mfma_f32_16x16x32_bf16 v[102:105], v[220:223], v[154:157], v[102:105]
	v_mfma_f32_16x16x32_bf16 v[98:101], v[228:231], v[154:157], v[98:101]
	v_mfma_f32_16x16x32_bf16 v[86:89], v[220:223], v[162:165], v[86:89]
	v_mfma_f32_16x16x32_bf16 v[82:85], v[228:231], v[162:165], v[82:85]
	v_mfma_f32_16x16x32_bf16 v[70:73], v[220:223], v[170:173], v[70:73]
	v_mfma_f32_16x16x32_bf16 v[66:69], v[228:231], v[170:173], v[66:69]
	v_mfma_f32_16x16x32_bf16 v[118:121], v[224:227], v[150:153], v[118:121]
	s_mov_b32 m0, s57
	v_mfma_f32_16x16x32_bf16 v[114:117], v[232:235], v[150:153], v[114:117]
	v_lshl_add_u64 v[236:237], v[240:241], 0, s[18:19]
	v_mfma_f32_16x16x32_bf16 v[102:105], v[224:227], v[158:161], v[102:105]
	v_mfma_f32_16x16x32_bf16 v[98:101], v[232:235], v[158:161], v[98:101]
	v_mfma_f32_16x16x32_bf16 v[86:89], v[224:227], v[166:169], v[86:89]
	v_mfma_f32_16x16x32_bf16 v[82:85], v[232:235], v[166:169], v[82:85]
	v_mfma_f32_16x16x32_bf16 v[70:73], v[224:227], v[174:177], v[70:73]
	v_mfma_f32_16x16x32_bf16 v[66:69], v[232:235], v[174:177], v[66:69]
	s_setprio 0
	s_barrier
	ds_read_b128 v[146:149], v216 offset:49152
	ds_read_b128 v[150:153], v216 offset:50176
	ds_read_b128 v[154:157], v216 offset:51200
	ds_read_b128 v[158:161], v216 offset:52224
	ds_read_b128 v[162:165], v216 offset:53248
	ds_read_b128 v[166:169], v216 offset:54272
	ds_read_b128 v[170:173], v216 offset:55296
	ds_read_b128 v[174:177], v216 offset:56320
	global_load_lds_dwordx4 v[236:237], off
	v_lshl_add_u64 v[236:237], v[242:243], 0, s[18:19]
	s_mov_b32 m0, s58
	s_nop 0
	global_load_lds_dwordx4 v[236:237], off
	s_setprio 1
	s_barrier
	s_waitcnt lgkmcnt(0)
	v_mfma_f32_16x16x32_bf16 v[62:65], v[130:133], v[146:149], v[62:65]
	v_mfma_f32_16x16x32_bf16 v[58:61], v[138:141], v[146:149], v[58:61]
	v_mfma_f32_16x16x32_bf16 v[46:49], v[130:133], v[154:157], v[46:49]
	v_mfma_f32_16x16x32_bf16 v[42:45], v[138:141], v[154:157], v[42:45]
	v_mfma_f32_16x16x32_bf16 v[30:33], v[130:133], v[162:165], v[30:33]
	v_mfma_f32_16x16x32_bf16 v[26:29], v[138:141], v[162:165], v[26:29]
	v_mfma_f32_16x16x32_bf16 v[14:17], v[130:133], v[170:173], v[14:17]
	v_mfma_f32_16x16x32_bf16 v[10:13], v[138:141], v[170:173], v[10:13]
	v_mfma_f32_16x16x32_bf16 v[62:65], v[134:137], v[150:153], v[62:65]
	v_mfma_f32_16x16x32_bf16 v[58:61], v[142:145], v[150:153], v[58:61]
	v_mfma_f32_16x16x32_bf16 v[46:49], v[134:137], v[158:161], v[46:49]
	v_mfma_f32_16x16x32_bf16 v[42:45], v[142:145], v[158:161], v[42:45]
	v_mfma_f32_16x16x32_bf16 v[30:33], v[134:137], v[166:169], v[30:33]
	v_mfma_f32_16x16x32_bf16 v[26:29], v[142:145], v[166:169], v[26:29]
	v_mfma_f32_16x16x32_bf16 v[14:17], v[134:137], v[174:177], v[14:17]
	v_mfma_f32_16x16x32_bf16 v[10:13], v[142:145], v[174:177], v[10:13]
	s_setprio 0
	s_barrier
	s_add_u32 s36, s36, 0x10080
	s_addc_u32 s37, s37, 0
	s_add_i32 s38, s39, s50
	v_lshl_add_u64 v[130:131], s[36:37], 0, v[178:179]
	s_mov_b32 m0, s38
	s_nop 0
	global_load_lds_dwordx4 v[130:131], off
	v_lshl_add_u64 v[130:131], s[36:37], 0, v[180:181]
	s_add_i32 m0, s38, 0x2000
	s_nop 0
	global_load_lds_dwordx4 v[130:131], off
	s_waitcnt vmcnt(6)
	s_setprio 1
	s_barrier
	v_mfma_f32_16x16x32_bf16 v[54:57], v[220:223], v[146:149], v[54:57]
	v_mfma_f32_16x16x32_bf16 v[50:53], v[228:231], v[146:149], v[50:53]
	v_mfma_f32_16x16x32_bf16 v[38:41], v[220:223], v[154:157], v[38:41]
	v_mfma_f32_16x16x32_bf16 v[34:37], v[228:231], v[154:157], v[34:37]
	v_mfma_f32_16x16x32_bf16 v[22:25], v[220:223], v[162:165], v[22:25]
	v_mfma_f32_16x16x32_bf16 v[18:21], v[228:231], v[162:165], v[18:21]
	v_mfma_f32_16x16x32_bf16 v[6:9], v[220:223], v[170:173], v[6:9]
	v_mfma_f32_16x16x32_bf16 v[2:5], v[228:231], v[170:173], v[2:5]
	v_mfma_f32_16x16x32_bf16 v[54:57], v[224:227], v[150:153], v[54:57]
	v_mfma_f32_16x16x32_bf16 v[50:53], v[232:235], v[150:153], v[50:53]
	v_mfma_f32_16x16x32_bf16 v[38:41], v[224:227], v[158:161], v[38:41]
	v_mfma_f32_16x16x32_bf16 v[34:37], v[232:235], v[158:161], v[34:37]
	v_mfma_f32_16x16x32_bf16 v[22:25], v[224:227], v[166:169], v[22:25]
	v_mfma_f32_16x16x32_bf16 v[18:21], v[232:235], v[166:169], v[18:21]
	v_mfma_f32_16x16x32_bf16 v[6:9], v[224:227], v[174:177], v[6:9]
	v_mfma_f32_16x16x32_bf16 v[2:5], v[232:235], v[174:177], v[2:5]
	s_setprio 0
	s_mov_b64 s[42:43], 0
	s_mov_b64 s[36:37], -1
	s_and_b64 vcc, exec, s[40:41]
	s_barrier
	s_cbranch_vccnz .LBB0_2618
	s_mov_b64 s[38:39], 0x100
	s_branch .LBB0_2614
	s_nop 0
	s_nop 0
	s_nop 0
	s_nop 0
